# in-proj GLA q/k epilogue: decay-table rows prefetched 4 row groups ahead through free registers
# baseline (speedup 1.0000x reference)
;     __device__ __forceinline__ void operator()(const f32x4 (&acc)[2][2][4][2], const Unit& u, int wr, int wc, int fr, int fq) const {
;     ...
;         } else if (u.pn < 16) {
;             const bool isq = u.pn < 14;
;             const int cb = (u.pn - (isq ? 12 : 14)) * 256;
;             bf16_t* d0 = (bf16_t*)(ws + (isq ? WS_QG : WS_KG));
;             f32x4 bc[2][2];
;     ...
;             BC_LOAD(0, 0);
; #pragma unroll
;             for (int g = 0; g < 16; ++g) {
;                 const int ai = g >> 3, m = (g >> 1) & 3, bj = g & 1;
;                 const int r = row0 + ai * HALF + m * 16;
;                 if (g + 1 < 16) BC_LOAD((g + 1) & 1, g + 1);
;                 {
;                     {
;                         const int col = cb + bj * HALF + lc;
;                         const size_t hoff = ((size_t)((r >> 11) * 4 + (col >> 7)) * SEQ + (r & (SEQ - 1))) * 128 + (col & 127);
;                         const f32x4 b0 = bc[g & 1][0], b1 = bc[g & 1][1];
;                         const f32x4 v0 = acc[ai][bj][m][0], v1 = acc[ai][bj][m][1];
;                         const float L2E = 1.4426950408889634f;
;                         if (isq) {
;                             const float s = 0.08838834764831845f;
;                             u32x4 o; o[0] = cvt_pk_bf16(v0[0] * s * __builtin_amdgcn_exp2f(b0[0] * L2E), v0[1] * s * __builtin_amdgcn_exp2f(b0[1] * L2E));
;                             o[1] = cvt_pk_bf16(v0[2] * s * __builtin_amdgcn_exp2f(b0[2] * L2E), v0[3] * s * __builtin_amdgcn_exp2f(b0[3] * L2E));
;                             o[2] = cvt_pk_bf16(v1[0] * s * __builtin_amdgcn_exp2f(b1[0] * L2E), v1[1] * s * __builtin_amdgcn_exp2f(b1[1] * L2E));
;                             o[3] = cvt_pk_bf16(v1[2] * s * __builtin_amdgcn_exp2f(b1[2] * L2E), v1[3] * s * __builtin_amdgcn_exp2f(b1[3] * L2E));
;                             __builtin_nontemporal_store(o, (u32x4*)(d0 + hoff));
;                         } else {
;                             u32x4 o;
;                             o[0] = cvt_pk_bf16(v0[0] * __builtin_amdgcn_exp2f(-b0[0] * L2E), v0[1] * __builtin_amdgcn_exp2f(-b0[1] * L2E));
;                             o[1] = cvt_pk_bf16(v0[2] * __builtin_amdgcn_exp2f(-b0[2] * L2E), v0[3] * __builtin_amdgcn_exp2f(-b0[3] * L2E));
.LBB0_356:
	s_and_b64 vcc, exec, s[2:3]
	s_cbranch_vccz .LBB0_571
	s_cmp_gt_u32 s78, 13
	s_cselect_b64 s[42:43], -1, 0
	s_cmp_lt_u32 s78, 14
	s_cselect_b64 s[2:3], -1, 0
	s_and_b64 s[8:9], s[2:3], exec
	s_cselect_b32 s10, -12, -14
	v_ashrrev_i32_e32 v193, 31, v192
	s_add_i32 s10, s10, s78
	v_lshlrev_b64 v[128:129], 11, v[192:193]
	v_lshl_or_b32 v168, s10, 8, v170
	v_lshl_add_u64 v[128:129], s[22:23], 0, v[128:129]
	v_lshl_add_u64 v[136:137], v[168:169], 2, v[128:129]
	v_mov_b32_e32 v206, v136
	v_mov_b32_e32 v207, v137
	global_load_dwordx4 v[132:135], v[136:137], off offset:16
	global_load_dwordx4 v[144:147], v[136:137], off
	global_load_dwordx4 v[128:131], v[136:137], off offset:528
	s_nop 0
	global_load_dwordx4 v[136:139], v[136:137], off offset:512
	s_mov_b32 s100, 0x8000
	s_mov_b32 s101, 0
	v_lshl_add_u64 v[204:205], v[206:207], 0, s[100:101]
	global_load_dwordx4 v[196:199], v[204:205], off offset:16
	global_load_dwordx4 v[200:203], v[204:205], off
	s_mov_b32 s100, 0x8000
	s_mov_b32 s101, 0
	v_lshl_add_u64 v[204:205], v[206:207], 0, s[100:101]
	global_load_dwordx4 v[214:217], v[204:205], off offset:528
	global_load_dwordx4 v[218:221], v[204:205], off offset:512
	s_mov_b32 s100, 0x10000
	s_mov_b32 s101, 0
	v_lshl_add_u64 v[204:205], v[206:207], 0, s[100:101]
	global_load_dwordx4 v[222:225], v[204:205], off offset:16
	global_load_dwordx4 v[226:229], v[204:205], off
	s_mov_b32 s100, 0x10000
	s_mov_b32 s101, 0
	v_lshl_add_u64 v[204:205], v[206:207], 0, s[100:101]
	global_load_dwordx4 v[230:233], v[204:205], off offset:528
	global_load_dwordx4 v[234:237], v[204:205], off offset:512
	s_mov_b64 s[8:9], -1
	s_and_b64 vcc, exec, s[42:43]
	s_cbranch_vccz .LBB0_359
	s_waitcnt vmcnt(10)
	v_mul_f32_e32 v140, 0xbfb8aa3b, v144
	v_mul_f32_e32 v141, 0xbfb8aa3b, v145
	v_exp_f32_e32 v140, v140
	v_exp_f32_e32 v141, v141
	s_mov_b64 s[8:9], 0
	v_mov_b32_e32 v149, v123
	v_pk_mul_f32 v[140:141], v[124:125], v[140:141]
	s_nop 0
	v_cvt_pk_bf16_f32 v140, v140, v141
	v_mul_f32_e32 v141, 0xbfb8aa3b, v146
	v_exp_f32_e32 v142, v141
	v_mul_f32_e32 v141, 0xbfb8aa3b, v147
	v_exp_f32_e32 v143, v141
	s_nop 0
	v_pk_mul_f32 v[142:143], v[126:127], v[142:143]
	s_nop 0
	v_cvt_pk_bf16_f32 v141, v142, v143
	v_mul_f32_e32 v142, 0xbfb8aa3b, v132
	v_mul_f32_e32 v143, 0xbfb8aa3b, v133
	v_exp_f32_e32 v142, v142
	v_exp_f32_e32 v143, v143
	s_nop 0
	v_pk_mul_f32 v[142:143], v[120:121], v[142:143]
	s_nop 0
	v_cvt_pk_bf16_f32 v142, v142, v143
	v_mul_f32_e32 v143, 0xbfb8aa3b, v134
	v_exp_f32_e32 v143, v143
	s_nop 0
	v_mul_f32_e32 v148, v122, v143
.LBB0_359:
	s_andn2_b64 vcc, exec, s[8:9]
	s_mov_b32 s8, 0xbfb8aa3b
	s_cbranch_vccnz .LBB0_361
	s_waitcnt vmcnt(10)
	v_mul_f32_e32 v140, 0x3fb8aa3b, v144
	v_mul_f32_e32 v141, 0x3fb8aa3b, v145
	v_exp_f32_e32 v140, v140
	v_exp_f32_e32 v141, v141
	v_pk_mul_f32 v[142:143], v[124:125], s[34:35] op_sel_hi:[1,0]
	v_mul_f32_e32 v132, 0x3fb8aa3b, v132
	v_mul_f32_e32 v133, 0x3fb8aa3b, v133
	v_pk_mul_f32 v[140:141], v[142:143], v[140:141]
	v_exp_f32_e32 v132, v132
	v_cvt_pk_bf16_f32 v140, v140, v141
	v_mul_f32_e32 v141, 0x3fb8aa3b, v146
	v_exp_f32_e32 v142, v141
	v_mul_f32_e32 v141, 0x3fb8aa3b, v147
	v_exp_f32_e32 v143, v141
	v_exp_f32_e32 v133, v133
	v_pk_mul_f32 v[144:145], v[126:127], s[34:35] op_sel_hi:[1,0]
	s_mov_b32 s8, 0x3fb8aa3b
	v_pk_mul_f32 v[142:143], v[144:145], v[142:143]
	s_nop 0
	v_cvt_pk_bf16_f32 v141, v142, v143
	v_pk_mul_f32 v[142:143], v[120:121], s[34:35] op_sel_hi:[1,0]
	s_nop 0
	v_pk_mul_f32 v[132:133], v[142:143], v[132:133]
	s_nop 0
	v_cvt_pk_bf16_f32 v142, v132, v133
	v_mul_f32_e32 v133, 0x3fb8aa3b, v134
	v_exp_f32_e32 v190, v133
	v_mul_f32_e32 v132, 0x3db504f3, v122
	v_mov_b32_e32 v133, v123
	v_pk_mul_f32 v[148:149], v[132:133], v[190:191]
.LBB0_361:
	s_and_b64 s[2:3], s[2:3], exec
	s_mov_b32 s2, 0x46188000
	s_cselect_b32 s2, s2, 0x47188000
	v_readlane_b32 s80, v252, 28
	v_readlane_b32 s81, v252, 29
	s_add_u32 s2, s80, s2
	s_addc_u32 s3, s81, 0
	s_ashr_i32 s9, s15, 9
	s_and_b32 s33, s9, -4
	s_lshl_b32 s17, s10, 1
	s_waitcnt vmcnt(10)
	v_mul_f32_e32 v132, s8, v135
	s_add_i32 s10, s33, s17
	v_exp_f32_e32 v132, v132
	s_ashr_i32 s11, s10, 31
	v_lshlrev_b32_e32 v133, 7, v192
	s_lshl_b64 s[8:9], s[10:11], 19
	v_and_b32_e32 v156, 0x3e780, v133
	s_add_u32 s10, s2, s8
	v_mul_f32_e32 v132, v149, v132
	s_addc_u32 s11, s3, s9
	v_lshlrev_b32_e32 v150, 1, v156
	v_mov_b32_e32 v151, v169
	v_cvt_pk_bf16_f32 v143, v148, v132
	v_lshl_add_u64 v[132:133], s[10:11], 0, v[150:151]
	v_lshlrev_b32_e32 v148, 1, v170
	v_mov_b32_e32 v149, v169
	v_lshl_add_u64 v[132:133], v[132:133], 0, v[148:149]
	global_store_dwordx4 v[132:133], v[140:143], off nt
	v_or_b32_e32 v132, 16, v192
	v_ashrrev_i32_e32 v133, 31, v132
	v_lshlrev_b64 v[132:133], 11, v[132:133]
	v_lshl_add_u64 v[132:133], s[22:23], 0, v[132:133]
	v_lshl_add_u64 v[152:153], v[168:169], 2, v[132:133]
	s_waitcnt vmcnt(7)
	v_mov_b32_e32 v132, v196
	v_mov_b32_e32 v133, v197
	v_mov_b32_e32 v134, v198
	v_mov_b32_e32 v135, v199
	v_mov_b32_e32 v140, v200
	v_mov_b32_e32 v141, v201
	v_mov_b32_e32 v142, v202
	v_mov_b32_e32 v143, v203
	s_mov_b32 s100, 0x18000
	s_mov_b32 s101, 0
	v_lshl_add_u64 v[204:205], v[206:207], 0, s[100:101]
	global_load_dwordx4 v[196:199], v[204:205], off offset:16
	global_load_dwordx4 v[200:203], v[204:205], off
	v_cndmask_b32_e64 v144, 0, 1, s[42:43]
	v_cmp_ne_u32_e64 s[8:9], 1, v144
	s_andn2_b64 vcc, exec, s[42:43]
	s_mov_b64 s[42:43], -1
	v_readlane_b32 s82, v252, 30
	v_readlane_b32 s83, v252, 31
	s_cbranch_vccnz .LBB0_363
	v_mul_f32_e32 v144, 0xbfb8aa3b, v136
	v_mul_f32_e32 v145, 0xbfb8aa3b, v137
	v_exp_f32_e32 v144, v144
	v_exp_f32_e32 v145, v145
	s_mov_b64 s[42:43], 0
	v_mov_b32_e32 v155, v115
	v_pk_mul_f32 v[144:145], v[116:117], v[144:145]
	s_nop 0
	v_cvt_pk_bf16_f32 v144, v144, v145
	v_mul_f32_e32 v145, 0xbfb8aa3b, v138
	v_exp_f32_e32 v146, v145
	v_mul_f32_e32 v145, 0xbfb8aa3b, v139
	v_exp_f32_e32 v147, v145
	s_nop 0
	v_pk_mul_f32 v[146:147], v[118:119], v[146:147]
	s_nop 0
	v_cvt_pk_bf16_f32 v145, v146, v147
	v_mul_f32_e32 v146, 0xbfb8aa3b, v128
	v_mul_f32_e32 v147, 0xbfb8aa3b, v129
	v_exp_f32_e32 v146, v146
	v_exp_f32_e32 v147, v147
	s_nop 0
	v_pk_mul_f32 v[146:147], v[112:113], v[146:147]
	s_nop 0
	v_cvt_pk_bf16_f32 v146, v146, v147
	v_mul_f32_e32 v147, 0xbfb8aa3b, v130
	v_exp_f32_e32 v147, v147
	s_nop 0
	v_mul_f32_e32 v154, v114, v147

;     __device__ __forceinline__ void operator()(const f32x4 (&acc)[2][2][4][2], const Unit& u, int wr, int wc, int fr, int fq) const {
;     ...
;         } else if (u.pn < 16) {
;             const bool isq = u.pn < 14;
;             const int cb = (u.pn - (isq ? 12 : 14)) * 256;
;             bf16_t* d0 = (bf16_t*)(ws + (isq ? WS_QG : WS_KG));
;             f32x4 bc[2][2];
;     ...
;             BC_LOAD(0, 0);
; #pragma unroll
;             for (int g = 0; g < 16; ++g) {
;                 const int ai = g >> 3, m = (g >> 1) & 3, bj = g & 1;
;                 const int r = row0 + ai * HALF + m * 16;
;                 if (g + 1 < 16) BC_LOAD((g + 1) & 1, g + 1);
;                 {
;                     {
;                         const int col = cb + bj * HALF + lc;
;                         const size_t hoff = ((size_t)((r >> 11) * 4 + (col >> 7)) * SEQ + (r & (SEQ - 1))) * 128 + (col & 127);
;                         const f32x4 b0 = bc[g & 1][0], b1 = bc[g & 1][1];
;                         const f32x4 v0 = acc[ai][bj][m][0], v1 = acc[ai][bj][m][1];
;                         const float L2E = 1.4426950408889634f;
;                         if (isq) {
;                             const float s = 0.08838834764831845f;
;                             u32x4 o; o[0] = cvt_pk_bf16(v0[0] * s * __builtin_amdgcn_exp2f(b0[0] * L2E), v0[1] * s * __builtin_amdgcn_exp2f(b0[1] * L2E));
;                             o[1] = cvt_pk_bf16(v0[2] * s * __builtin_amdgcn_exp2f(b0[2] * L2E), v0[3] * s * __builtin_amdgcn_exp2f(b0[3] * L2E));
;                             o[2] = cvt_pk_bf16(v1[0] * s * __builtin_amdgcn_exp2f(b1[0] * L2E), v1[1] * s * __builtin_amdgcn_exp2f(b1[1] * L2E));
;                             o[3] = cvt_pk_bf16(v1[2] * s * __builtin_amdgcn_exp2f(b1[2] * L2E), v1[3] * s * __builtin_amdgcn_exp2f(b1[3] * L2E));
;                             __builtin_nontemporal_store(o, (u32x4*)(d0 + hoff));
;                         } else {
;                             u32x4 o;
;                             o[0] = cvt_pk_bf16(v0[0] * __builtin_amdgcn_exp2f(-b0[0] * L2E), v0[1] * __builtin_amdgcn_exp2f(-b0[1] * L2E));
;                             o[1] = cvt_pk_bf16(v0[2] * __builtin_amdgcn_exp2f(-b0[2] * L2E), v0[3] * __builtin_amdgcn_exp2f(-b0[3] * L2E));
.LBB0_365:
	v_mul_f32_e32 v128, s18, v131
	s_or_b32 s18, s17, 1
	v_exp_f32_e32 v128, v128
	s_add_i32 s42, s33, s18
	s_ashr_i32 s43, s42, 31
	s_lshl_b64 s[42:43], s[42:43], 19
	s_add_u32 s42, s2, s42
	v_mul_f32_e32 v128, v155, v128
	s_addc_u32 s43, s3, s43
	v_mov_b32_e32 v151, v169
	v_cvt_pk_bf16_f32 v147, v154, v128
	v_lshl_add_u64 v[128:129], s[42:43], 0, v[150:151]
	v_mov_b32_e32 v149, v169
	v_lshl_add_u64 v[128:129], v[128:129], 0, v[148:149]
	global_store_dwordx4 v[128:129], v[144:147], off nt
	s_waitcnt vmcnt(8)
	v_mov_b32_e32 v128, v214
	v_mov_b32_e32 v129, v215
	v_mov_b32_e32 v130, v216
	v_mov_b32_e32 v131, v217
	v_mov_b32_e32 v136, v218
	v_mov_b32_e32 v137, v219
	v_mov_b32_e32 v138, v220
	v_mov_b32_e32 v139, v221
	s_mov_b32 s100, 0x18000
	s_mov_b32 s101, 0
	v_lshl_add_u64 v[204:205], v[206:207], 0, s[100:101]
	global_load_dwordx4 v[214:217], v[204:205], off offset:528
	global_load_dwordx4 v[218:221], v[204:205], off offset:512
	s_nop 0
	s_and_b64 vcc, exec, s[8:9]
	s_mov_b64 s[54:55], -1
	s_cbranch_vccnz .LBB0_367
	v_mul_f32_e32 v144, 0xbfb8aa3b, v140
	v_mul_f32_e32 v145, 0xbfb8aa3b, v141
	v_exp_f32_e32 v144, v144
	v_exp_f32_e32 v145, v145
	s_mov_b64 s[54:55], 0
	v_mov_b32_e32 v153, v107
	v_pk_mul_f32 v[144:145], v[108:109], v[144:145]
	s_nop 0
	v_cvt_pk_bf16_f32 v144, v144, v145
	v_mul_f32_e32 v145, 0xbfb8aa3b, v142
	v_exp_f32_e32 v146, v145
	v_mul_f32_e32 v145, 0xbfb8aa3b, v143
	v_exp_f32_e32 v147, v145
	s_nop 0
	v_pk_mul_f32 v[146:147], v[110:111], v[146:147]
	s_nop 0
	v_cvt_pk_bf16_f32 v145, v146, v147
	v_mul_f32_e32 v146, 0xbfb8aa3b, v132
	v_mul_f32_e32 v147, 0xbfb8aa3b, v133
	v_exp_f32_e32 v146, v146
	v_exp_f32_e32 v147, v147
	s_nop 0
	v_pk_mul_f32 v[146:147], v[104:105], v[146:147]
	s_nop 0
	v_cvt_pk_bf16_f32 v146, v146, v147
	v_mul_f32_e32 v147, 0xbfb8aa3b, v134
	v_exp_f32_e32 v147, v147
	s_nop 0
	v_mul_f32_e32 v152, v106, v147
.LBB0_367:
	s_andn2_b64 vcc, exec, s[54:55]
	s_mov_b32 s33, 0xbfb8aa3b
	s_cbranch_vccnz .LBB0_369
	v_mul_f32_e32 v140, 0x3fb8aa3b, v140
	v_mul_f32_e32 v141, 0x3fb8aa3b, v141
	v_exp_f32_e32 v140, v140
	v_exp_f32_e32 v141, v141
	v_pk_mul_f32 v[144:145], v[108:109], s[34:35] op_sel_hi:[1,0]
	v_mul_f32_e32 v132, 0x3fb8aa3b, v132
	v_mul_f32_e32 v133, 0x3fb8aa3b, v133
	v_pk_mul_f32 v[140:141], v[144:145], v[140:141]
	v_exp_f32_e32 v132, v132
	v_cvt_pk_bf16_f32 v144, v140, v141
	v_mul_f32_e32 v140, 0x3fb8aa3b, v142
	v_mul_f32_e32 v141, 0x3fb8aa3b, v143
	v_exp_f32_e32 v140, v140
	v_exp_f32_e32 v141, v141
	v_exp_f32_e32 v133, v133
	v_pk_mul_f32 v[142:143], v[110:111], s[34:35] op_sel_hi:[1,0]
	s_mov_b32 s33, 0x3fb8aa3b
	v_pk_mul_f32 v[140:141], v[142:143], v[140:141]
	s_nop 0
	v_cvt_pk_bf16_f32 v145, v140, v141
	v_pk_mul_f32 v[140:141], v[104:105], s[34:35] op_sel_hi:[1,0]
	s_nop 0
	v_pk_mul_f32 v[132:133], v[140:141], v[132:133]
	s_nop 0
	v_cvt_pk_bf16_f32 v146, v132, v133
	v_mul_f32_e32 v133, 0x3fb8aa3b, v134
	v_exp_f32_e32 v190, v133
	v_mul_f32_e32 v132, 0x3db504f3, v106
	v_mov_b32_e32 v133, v107
	v_pk_mul_f32 v[152:153], v[132:133], v[190:191]
.LBB0_369:
	v_mul_f32_e32 v132, s33, v135
	v_exp_f32_e32 v132, v132
	v_or_b32_e32 v133, 0x800, v156
	v_mov_b32_e32 v151, v169
	v_lshlrev_b32_e32 v150, 1, v133
	v_mul_f32_e32 v132, v153, v132
	v_cvt_pk_bf16_f32 v147, v152, v132
	v_lshl_add_u64 v[132:133], s[10:11], 0, v[150:151]
	v_mov_b32_e32 v149, v169
	v_lshl_add_u64 v[132:133], v[132:133], 0, v[148:149]
	global_store_dwordx4 v[132:133], v[144:147], off nt
	v_or_b32_e32 v132, 32, v192
	v_ashrrev_i32_e32 v133, 31, v132
	v_lshlrev_b64 v[132:133], 11, v[132:133]
	v_lshl_add_u64 v[132:133], s[22:23], 0, v[132:133]
	v_lshl_add_u64 v[152:153], v[168:169], 2, v[132:133]
	s_waitcnt vmcnt(9)
	v_mov_b32_e32 v132, v222
	v_mov_b32_e32 v133, v223
	v_mov_b32_e32 v134, v224
	v_mov_b32_e32 v135, v225
	v_mov_b32_e32 v140, v226
	v_mov_b32_e32 v141, v227
	v_mov_b32_e32 v142, v228
	v_mov_b32_e32 v143, v229
	s_mov_b32 s100, 0x40000
	s_mov_b32 s101, 0
	v_lshl_add_u64 v[204:205], v[206:207], 0, s[100:101]
	global_load_dwordx4 v[222:225], v[204:205], off offset:16
	global_load_dwordx4 v[226:229], v[204:205], off
	s_and_b64 vcc, exec, s[8:9]
	s_mov_b64 s[54:55], -1
	s_cbranch_vccnz .LBB0_371
	v_mul_f32_e32 v144, 0xbfb8aa3b, v136
	v_mul_f32_e32 v145, 0xbfb8aa3b, v137
	v_exp_f32_e32 v144, v144
	v_exp_f32_e32 v145, v145
	s_mov_b64 s[54:55], 0
	v_mov_b32_e32 v155, v99
	v_pk_mul_f32 v[144:145], v[100:101], v[144:145]
	s_nop 0
	v_cvt_pk_bf16_f32 v144, v144, v145
	v_mul_f32_e32 v145, 0xbfb8aa3b, v138
	v_exp_f32_e32 v146, v145
	v_mul_f32_e32 v145, 0xbfb8aa3b, v139
	v_exp_f32_e32 v147, v145
	s_nop 0
	v_pk_mul_f32 v[146:147], v[102:103], v[146:147]
	s_nop 0
	v_cvt_pk_bf16_f32 v145, v146, v147
	v_mul_f32_e32 v146, 0xbfb8aa3b, v128
	v_mul_f32_e32 v147, 0xbfb8aa3b, v129
	v_exp_f32_e32 v146, v146
	v_exp_f32_e32 v147, v147
	s_nop 0
	v_pk_mul_f32 v[146:147], v[96:97], v[146:147]
	s_nop 0
	v_cvt_pk_bf16_f32 v146, v146, v147
	v_mul_f32_e32 v147, 0xbfb8aa3b, v130
	v_exp_f32_e32 v147, v147
	s_nop 0
	v_mul_f32_e32 v154, v98, v147

;     __device__ __forceinline__ void operator()(const f32x4 (&acc)[2][2][4][2], const Unit& u, int wr, int wc, int fr, int fq) const {
;     ...
;         } else if (u.pn < 16) {
;             const bool isq = u.pn < 14;
;             const int cb = (u.pn - (isq ? 12 : 14)) * 256;
;             bf16_t* d0 = (bf16_t*)(ws + (isq ? WS_QG : WS_KG));
;             f32x4 bc[2][2];
;     ...
;             BC_LOAD(0, 0);
; #pragma unroll
;             for (int g = 0; g < 16; ++g) {
;                 const int ai = g >> 3, m = (g >> 1) & 3, bj = g & 1;
;                 const int r = row0 + ai * HALF + m * 16;
;                 if (g + 1 < 16) BC_LOAD((g + 1) & 1, g + 1);
;                 {
;                     {
;                         const int col = cb + bj * HALF + lc;
;                         const size_t hoff = ((size_t)((r >> 11) * 4 + (col >> 7)) * SEQ + (r & (SEQ - 1))) * 128 + (col & 127);
;                         const f32x4 b0 = bc[g & 1][0], b1 = bc[g & 1][1];
;                         const f32x4 v0 = acc[ai][bj][m][0], v1 = acc[ai][bj][m][1];
;                         const float L2E = 1.4426950408889634f;
;                         if (isq) {
;                             const float s = 0.08838834764831845f;
;                             u32x4 o; o[0] = cvt_pk_bf16(v0[0] * s * __builtin_amdgcn_exp2f(b0[0] * L2E), v0[1] * s * __builtin_amdgcn_exp2f(b0[1] * L2E));
;                             o[1] = cvt_pk_bf16(v0[2] * s * __builtin_amdgcn_exp2f(b0[2] * L2E), v0[3] * s * __builtin_amdgcn_exp2f(b0[3] * L2E));
;                             o[2] = cvt_pk_bf16(v1[0] * s * __builtin_amdgcn_exp2f(b1[0] * L2E), v1[1] * s * __builtin_amdgcn_exp2f(b1[1] * L2E));
;                             o[3] = cvt_pk_bf16(v1[2] * s * __builtin_amdgcn_exp2f(b1[2] * L2E), v1[3] * s * __builtin_amdgcn_exp2f(b1[3] * L2E));
;                             __builtin_nontemporal_store(o, (u32x4*)(d0 + hoff));
;                         } else {
;                             u32x4 o;
;                             o[0] = cvt_pk_bf16(v0[0] * __builtin_amdgcn_exp2f(-b0[0] * L2E), v0[1] * __builtin_amdgcn_exp2f(-b0[1] * L2E));
;                             o[1] = cvt_pk_bf16(v0[2] * __builtin_amdgcn_exp2f(-b0[2] * L2E), v0[3] * __builtin_amdgcn_exp2f(-b0[3] * L2E));
.LBB0_373:
	v_mul_f32_e32 v128, s33, v131
	v_exp_f32_e32 v130, v128
	v_mov_b32_e32 v151, v169
	v_mov_b32_e32 v149, v169
	v_lshl_add_u64 v[128:129], s[42:43], 0, v[150:151]
	v_mul_f32_e32 v130, v155, v130
	v_cvt_pk_bf16_f32 v147, v154, v130
	v_lshl_add_u64 v[128:129], v[128:129], 0, v[148:149]
	global_store_dwordx4 v[128:129], v[144:147], off nt
	s_waitcnt vmcnt(10)
	v_mov_b32_e32 v128, v230
	v_mov_b32_e32 v129, v231
	v_mov_b32_e32 v130, v232
	v_mov_b32_e32 v131, v233
	v_mov_b32_e32 v136, v234
	v_mov_b32_e32 v137, v235
	v_mov_b32_e32 v138, v236
	v_mov_b32_e32 v139, v237
	s_mov_b32 s100, 0x40000
	s_mov_b32 s101, 0
	v_lshl_add_u64 v[204:205], v[206:207], 0, s[100:101]
	global_load_dwordx4 v[230:233], v[204:205], off offset:528
	global_load_dwordx4 v[234:237], v[204:205], off offset:512
	s_nop 0
	s_and_b64 vcc, exec, s[8:9]
	s_mov_b64 s[54:55], -1
	s_cbranch_vccnz .LBB0_375
	v_mul_f32_e32 v144, 0xbfb8aa3b, v140
	v_mul_f32_e32 v145, 0xbfb8aa3b, v141
	v_exp_f32_e32 v144, v144
	v_exp_f32_e32 v145, v145
	s_mov_b64 s[54:55], 0
	v_mov_b32_e32 v153, v91
	v_pk_mul_f32 v[144:145], v[92:93], v[144:145]
	s_nop 0
	v_cvt_pk_bf16_f32 v144, v144, v145
	v_mul_f32_e32 v145, 0xbfb8aa3b, v142
	v_exp_f32_e32 v146, v145
	v_mul_f32_e32 v145, 0xbfb8aa3b, v143
	v_exp_f32_e32 v147, v145
	s_nop 0
	v_pk_mul_f32 v[146:147], v[94:95], v[146:147]
	s_nop 0
	v_cvt_pk_bf16_f32 v145, v146, v147
	v_mul_f32_e32 v146, 0xbfb8aa3b, v132
	v_mul_f32_e32 v147, 0xbfb8aa3b, v133
	v_exp_f32_e32 v146, v146
	v_exp_f32_e32 v147, v147
	s_nop 0
	v_pk_mul_f32 v[146:147], v[88:89], v[146:147]
	s_nop 0
	v_cvt_pk_bf16_f32 v146, v146, v147
	v_mul_f32_e32 v147, 0xbfb8aa3b, v134
	v_exp_f32_e32 v147, v147
	s_nop 0
	v_mul_f32_e32 v152, v90, v147
.LBB0_375:
	s_andn2_b64 vcc, exec, s[54:55]
	s_mov_b32 s33, 0xbfb8aa3b
	s_cbranch_vccnz .LBB0_377
	v_mul_f32_e32 v140, 0x3fb8aa3b, v140
	v_mul_f32_e32 v141, 0x3fb8aa3b, v141
	v_exp_f32_e32 v140, v140
	v_exp_f32_e32 v141, v141
	v_pk_mul_f32 v[144:145], v[92:93], s[34:35] op_sel_hi:[1,0]
	v_mul_f32_e32 v132, 0x3fb8aa3b, v132
	v_mul_f32_e32 v133, 0x3fb8aa3b, v133
	v_pk_mul_f32 v[140:141], v[144:145], v[140:141]
	v_exp_f32_e32 v132, v132
	v_cvt_pk_bf16_f32 v144, v140, v141
	v_mul_f32_e32 v140, 0x3fb8aa3b, v142
	v_mul_f32_e32 v141, 0x3fb8aa3b, v143
	v_exp_f32_e32 v140, v140
	v_exp_f32_e32 v141, v141
	v_exp_f32_e32 v133, v133
	v_pk_mul_f32 v[142:143], v[94:95], s[34:35] op_sel_hi:[1,0]
	s_mov_b32 s33, 0x3fb8aa3b
	v_pk_mul_f32 v[140:141], v[142:143], v[140:141]
	s_nop 0
	v_cvt_pk_bf16_f32 v145, v140, v141
	v_pk_mul_f32 v[140:141], v[88:89], s[34:35] op_sel_hi:[1,0]
	s_nop 0
	v_pk_mul_f32 v[132:133], v[140:141], v[132:133]
	s_nop 0
	v_cvt_pk_bf16_f32 v146, v132, v133
	v_mul_f32_e32 v133, 0x3fb8aa3b, v134
	v_exp_f32_e32 v190, v133
	v_mul_f32_e32 v132, 0x3db504f3, v90
	v_mov_b32_e32 v133, v91
	v_pk_mul_f32 v[152:153], v[132:133], v[190:191]
.LBB0_377:
	v_mul_f32_e32 v132, s33, v135
	v_exp_f32_e32 v132, v132
	v_or_b32_e32 v133, 0x1000, v156
	v_mov_b32_e32 v151, v169
	v_lshlrev_b32_e32 v150, 1, v133
	v_mul_f32_e32 v132, v153, v132
	v_cvt_pk_bf16_f32 v147, v152, v132
	v_lshl_add_u64 v[132:133], s[10:11], 0, v[150:151]
	v_mov_b32_e32 v149, v169
	v_lshl_add_u64 v[132:133], v[132:133], 0, v[148:149]
	global_store_dwordx4 v[132:133], v[144:147], off nt
	v_or_b32_e32 v132, 48, v192
	v_ashrrev_i32_e32 v133, 31, v132
	v_lshlrev_b64 v[132:133], 11, v[132:133]
	v_lshl_add_u64 v[132:133], s[22:23], 0, v[132:133]
	v_lshl_add_u64 v[152:153], v[168:169], 2, v[132:133]
	s_waitcnt vmcnt(10)
	v_mov_b32_e32 v132, v196
	v_mov_b32_e32 v133, v197
	v_mov_b32_e32 v134, v198
	v_mov_b32_e32 v135, v199
	v_mov_b32_e32 v140, v200
	v_mov_b32_e32 v141, v201
	v_mov_b32_e32 v142, v202
	v_mov_b32_e32 v143, v203
	s_mov_b32 s100, 0x48000
	s_mov_b32 s101, 0
	v_lshl_add_u64 v[204:205], v[206:207], 0, s[100:101]
	global_load_dwordx4 v[196:199], v[204:205], off offset:16
	global_load_dwordx4 v[200:203], v[204:205], off
	s_and_b64 vcc, exec, s[8:9]
	s_mov_b64 s[54:55], -1
	s_cbranch_vccnz .LBB0_379
	v_mul_f32_e32 v144, 0xbfb8aa3b, v136
	v_mul_f32_e32 v145, 0xbfb8aa3b, v137
	v_exp_f32_e32 v144, v144
	v_exp_f32_e32 v145, v145
	s_mov_b64 s[54:55], 0
	v_mov_b32_e32 v155, v83
	v_pk_mul_f32 v[144:145], v[84:85], v[144:145]
	s_nop 0
	v_cvt_pk_bf16_f32 v144, v144, v145
	v_mul_f32_e32 v145, 0xbfb8aa3b, v138
	v_exp_f32_e32 v146, v145
	v_mul_f32_e32 v145, 0xbfb8aa3b, v139
	v_exp_f32_e32 v147, v145
	s_nop 0
	v_pk_mul_f32 v[146:147], v[86:87], v[146:147]
	s_nop 0
	v_cvt_pk_bf16_f32 v145, v146, v147
	v_mul_f32_e32 v146, 0xbfb8aa3b, v128
	v_mul_f32_e32 v147, 0xbfb8aa3b, v129
	v_exp_f32_e32 v146, v146
	v_exp_f32_e32 v147, v147
	s_nop 0
	v_pk_mul_f32 v[146:147], v[80:81], v[146:147]
	s_nop 0
	v_cvt_pk_bf16_f32 v146, v146, v147
	v_mul_f32_e32 v147, 0xbfb8aa3b, v130
	v_exp_f32_e32 v147, v147
	s_nop 0
	v_mul_f32_e32 v154, v82, v147

;     __device__ __forceinline__ void operator()(const f32x4 (&acc)[2][2][4][2], const Unit& u, int wr, int wc, int fr, int fq) const {
;     ...
;         } else if (u.pn < 16) {
;             const bool isq = u.pn < 14;
;             const int cb = (u.pn - (isq ? 12 : 14)) * 256;
;             bf16_t* d0 = (bf16_t*)(ws + (isq ? WS_QG : WS_KG));
;             f32x4 bc[2][2];
;     ...
;             BC_LOAD(0, 0);
; #pragma unroll
;             for (int g = 0; g < 16; ++g) {
;                 const int ai = g >> 3, m = (g >> 1) & 3, bj = g & 1;
;                 const int r = row0 + ai * HALF + m * 16;
;                 if (g + 1 < 16) BC_LOAD((g + 1) & 1, g + 1);
;                 {
;                     {
;                         const int col = cb + bj * HALF + lc;
;                         const size_t hoff = ((size_t)((r >> 11) * 4 + (col >> 7)) * SEQ + (r & (SEQ - 1))) * 128 + (col & 127);
;                         const f32x4 b0 = bc[g & 1][0], b1 = bc[g & 1][1];
;                         const f32x4 v0 = acc[ai][bj][m][0], v1 = acc[ai][bj][m][1];
;                         const float L2E = 1.4426950408889634f;
;                         if (isq) {
;                             const float s = 0.08838834764831845f;
;                             u32x4 o; o[0] = cvt_pk_bf16(v0[0] * s * __builtin_amdgcn_exp2f(b0[0] * L2E), v0[1] * s * __builtin_amdgcn_exp2f(b0[1] * L2E));
;                             o[1] = cvt_pk_bf16(v0[2] * s * __builtin_amdgcn_exp2f(b0[2] * L2E), v0[3] * s * __builtin_amdgcn_exp2f(b0[3] * L2E));
;                             o[2] = cvt_pk_bf16(v1[0] * s * __builtin_amdgcn_exp2f(b1[0] * L2E), v1[1] * s * __builtin_amdgcn_exp2f(b1[1] * L2E));
;                             o[3] = cvt_pk_bf16(v1[2] * s * __builtin_amdgcn_exp2f(b1[2] * L2E), v1[3] * s * __builtin_amdgcn_exp2f(b1[3] * L2E));
;                             __builtin_nontemporal_store(o, (u32x4*)(d0 + hoff));
;                         } else {
;                             u32x4 o;
;                             o[0] = cvt_pk_bf16(v0[0] * __builtin_amdgcn_exp2f(-b0[0] * L2E), v0[1] * __builtin_amdgcn_exp2f(-b0[1] * L2E));
;                             o[1] = cvt_pk_bf16(v0[2] * __builtin_amdgcn_exp2f(-b0[2] * L2E), v0[3] * __builtin_amdgcn_exp2f(-b0[3] * L2E));
.LBB0_381:
	v_mul_f32_e32 v128, s33, v131
	v_exp_f32_e32 v130, v128
	v_mov_b32_e32 v151, v169
	v_mov_b32_e32 v149, v169
	v_lshl_add_u64 v[128:129], s[42:43], 0, v[150:151]
	v_mul_f32_e32 v130, v155, v130
	v_cvt_pk_bf16_f32 v147, v154, v130
	v_lshl_add_u64 v[128:129], v[128:129], 0, v[148:149]
	global_store_dwordx4 v[128:129], v[144:147], off nt
	s_waitcnt vmcnt(10)
	v_mov_b32_e32 v128, v214
	v_mov_b32_e32 v129, v215
	v_mov_b32_e32 v130, v216
	v_mov_b32_e32 v131, v217
	v_mov_b32_e32 v136, v218
	v_mov_b32_e32 v137, v219
	v_mov_b32_e32 v138, v220
	v_mov_b32_e32 v139, v221
	s_mov_b32 s100, 0x48000
	s_mov_b32 s101, 0
	v_lshl_add_u64 v[204:205], v[206:207], 0, s[100:101]
	global_load_dwordx4 v[214:217], v[204:205], off offset:528
	global_load_dwordx4 v[218:221], v[204:205], off offset:512
	s_nop 0
	s_and_b64 vcc, exec, s[8:9]
	s_mov_b64 s[54:55], -1
	s_cbranch_vccnz .LBB0_383
	v_mul_f32_e32 v144, 0xbfb8aa3b, v140
	v_mul_f32_e32 v145, 0xbfb8aa3b, v141
	v_exp_f32_e32 v144, v144
	v_exp_f32_e32 v145, v145
	s_mov_b64 s[54:55], 0
	v_mov_b32_e32 v151, v75
	v_pk_mul_f32 v[144:145], v[76:77], v[144:145]
	s_nop 0
	v_cvt_pk_bf16_f32 v144, v144, v145
	v_mul_f32_e32 v145, 0xbfb8aa3b, v142
	v_exp_f32_e32 v146, v145
	v_mul_f32_e32 v145, 0xbfb8aa3b, v143
	v_exp_f32_e32 v147, v145
	s_nop 0
	v_pk_mul_f32 v[146:147], v[78:79], v[146:147]
	s_nop 0
	v_cvt_pk_bf16_f32 v145, v146, v147
	v_mul_f32_e32 v146, 0xbfb8aa3b, v132
	v_mul_f32_e32 v147, 0xbfb8aa3b, v133
	v_exp_f32_e32 v146, v146
	v_exp_f32_e32 v147, v147
	s_nop 0
	v_pk_mul_f32 v[146:147], v[72:73], v[146:147]
	s_nop 0
	v_cvt_pk_bf16_f32 v146, v146, v147
	v_mul_f32_e32 v147, 0xbfb8aa3b, v134
	v_exp_f32_e32 v147, v147
	s_nop 0
	v_mul_f32_e32 v150, v74, v147
.LBB0_383:
	s_andn2_b64 vcc, exec, s[54:55]
	s_mov_b32 s33, 0xbfb8aa3b
	s_cbranch_vccnz .LBB0_385
	v_mul_f32_e32 v140, 0x3fb8aa3b, v140
	v_mul_f32_e32 v141, 0x3fb8aa3b, v141
	v_exp_f32_e32 v140, v140
	v_exp_f32_e32 v141, v141
	v_pk_mul_f32 v[144:145], v[76:77], s[34:35] op_sel_hi:[1,0]
	v_mul_f32_e32 v132, 0x3fb8aa3b, v132
	v_mul_f32_e32 v133, 0x3fb8aa3b, v133
	v_pk_mul_f32 v[140:141], v[144:145], v[140:141]
	v_exp_f32_e32 v132, v132
	v_cvt_pk_bf16_f32 v144, v140, v141
	v_mul_f32_e32 v140, 0x3fb8aa3b, v142
	v_mul_f32_e32 v141, 0x3fb8aa3b, v143
	v_exp_f32_e32 v140, v140
	v_exp_f32_e32 v141, v141
	v_exp_f32_e32 v133, v133
	v_pk_mul_f32 v[142:143], v[78:79], s[34:35] op_sel_hi:[1,0]
	s_mov_b32 s33, 0x3fb8aa3b
	v_pk_mul_f32 v[140:141], v[142:143], v[140:141]
	s_nop 0
	v_cvt_pk_bf16_f32 v145, v140, v141
	v_pk_mul_f32 v[140:141], v[72:73], s[34:35] op_sel_hi:[1,0]
	s_nop 0
	v_pk_mul_f32 v[132:133], v[140:141], v[132:133]
	s_nop 0
	v_cvt_pk_bf16_f32 v146, v132, v133
	v_mul_f32_e32 v133, 0x3fb8aa3b, v134
	v_exp_f32_e32 v190, v133
	v_mul_f32_e32 v132, 0x3db504f3, v74
	v_mov_b32_e32 v133, v75
	v_pk_mul_f32 v[150:151], v[132:133], v[190:191]
.LBB0_385:
	v_mul_f32_e32 v132, s33, v135
	v_exp_f32_e32 v132, v132
	v_or_b32_e32 v133, 0x1800, v156
	v_mov_b32_e32 v153, v169
	v_lshlrev_b32_e32 v152, 1, v133
	v_mul_f32_e32 v132, v151, v132
	v_cvt_pk_bf16_f32 v147, v150, v132
	v_lshl_add_u64 v[132:133], s[10:11], 0, v[152:153]
	v_mov_b32_e32 v149, v169
	v_add_u32_e32 v150, 0x80, v192
	v_lshl_add_u64 v[132:133], v[132:133], 0, v[148:149]
	v_ashrrev_i32_e32 v151, 31, v150
	global_store_dwordx4 v[132:133], v[144:147], off nt
	v_lshlrev_b64 v[132:133], 11, v[150:151]
	v_lshl_add_u64 v[132:133], s[22:23], 0, v[132:133]
	v_lshl_add_u64 v[154:155], v[168:169], 2, v[132:133]
	s_waitcnt vmcnt(10)
	v_mov_b32_e32 v132, v222
	v_mov_b32_e32 v133, v223
	v_mov_b32_e32 v134, v224
	v_mov_b32_e32 v135, v225
	v_mov_b32_e32 v140, v226
	v_mov_b32_e32 v141, v227
	v_mov_b32_e32 v142, v228
	v_mov_b32_e32 v143, v229
	s_mov_b32 s100, 0x50000
	s_mov_b32 s101, 0
	v_lshl_add_u64 v[204:205], v[206:207], 0, s[100:101]
	global_load_dwordx4 v[222:225], v[204:205], off offset:16
	global_load_dwordx4 v[226:229], v[204:205], off
	s_and_b64 vcc, exec, s[8:9]
	s_mov_b64 s[10:11], -1
	s_cbranch_vccnz .LBB0_387
	v_mul_f32_e32 v144, 0xbfb8aa3b, v136
	v_mul_f32_e32 v145, 0xbfb8aa3b, v137
	v_exp_f32_e32 v144, v144
	v_exp_f32_e32 v145, v145
	s_mov_b64 s[10:11], 0
	v_mov_b32_e32 v157, v67
	v_pk_mul_f32 v[144:145], v[68:69], v[144:145]
	s_nop 0
	v_cvt_pk_bf16_f32 v144, v144, v145
	v_mul_f32_e32 v145, 0xbfb8aa3b, v138
	v_exp_f32_e32 v146, v145
	v_mul_f32_e32 v145, 0xbfb8aa3b, v139
	v_exp_f32_e32 v147, v145
	s_nop 0
	v_pk_mul_f32 v[146:147], v[70:71], v[146:147]
	s_nop 0
	v_cvt_pk_bf16_f32 v145, v146, v147
	v_mul_f32_e32 v146, 0xbfb8aa3b, v128
	v_mul_f32_e32 v147, 0xbfb8aa3b, v129
	v_exp_f32_e32 v146, v146
	v_exp_f32_e32 v147, v147
	s_nop 0
	v_pk_mul_f32 v[146:147], v[64:65], v[146:147]
	s_nop 0
	v_cvt_pk_bf16_f32 v146, v146, v147
	v_mul_f32_e32 v147, 0xbfb8aa3b, v130
	v_exp_f32_e32 v147, v147
	s_nop 0
	v_mul_f32_e32 v156, v66, v147

;     __device__ __forceinline__ void operator()(const f32x4 (&acc)[2][2][4][2], const Unit& u, int wr, int wc, int fr, int fq) const {
;     ...
;         } else if (u.pn < 16) {
;             const bool isq = u.pn < 14;
;             const int cb = (u.pn - (isq ? 12 : 14)) * 256;
;             bf16_t* d0 = (bf16_t*)(ws + (isq ? WS_QG : WS_KG));
;             f32x4 bc[2][2];
;     ...
;             BC_LOAD(0, 0);
; #pragma unroll
;             for (int g = 0; g < 16; ++g) {
;                 const int ai = g >> 3, m = (g >> 1) & 3, bj = g & 1;
;                 const int r = row0 + ai * HALF + m * 16;
;                 if (g + 1 < 16) BC_LOAD((g + 1) & 1, g + 1);
;                 {
;                     {
;                         const int col = cb + bj * HALF + lc;
;                         const size_t hoff = ((size_t)((r >> 11) * 4 + (col >> 7)) * SEQ + (r & (SEQ - 1))) * 128 + (col & 127);
;                         const f32x4 b0 = bc[g & 1][0], b1 = bc[g & 1][1];
;                         const f32x4 v0 = acc[ai][bj][m][0], v1 = acc[ai][bj][m][1];
;                         const float L2E = 1.4426950408889634f;
;                         if (isq) {
;                             const float s = 0.08838834764831845f;
;                             u32x4 o; o[0] = cvt_pk_bf16(v0[0] * s * __builtin_amdgcn_exp2f(b0[0] * L2E), v0[1] * s * __builtin_amdgcn_exp2f(b0[1] * L2E));
;                             o[1] = cvt_pk_bf16(v0[2] * s * __builtin_amdgcn_exp2f(b0[2] * L2E), v0[3] * s * __builtin_amdgcn_exp2f(b0[3] * L2E));
;                             o[2] = cvt_pk_bf16(v1[0] * s * __builtin_amdgcn_exp2f(b1[0] * L2E), v1[1] * s * __builtin_amdgcn_exp2f(b1[1] * L2E));
;                             o[3] = cvt_pk_bf16(v1[2] * s * __builtin_amdgcn_exp2f(b1[2] * L2E), v1[3] * s * __builtin_amdgcn_exp2f(b1[3] * L2E));
;                             __builtin_nontemporal_store(o, (u32x4*)(d0 + hoff));
;                         } else {
;                             u32x4 o;
;                             o[0] = cvt_pk_bf16(v0[0] * __builtin_amdgcn_exp2f(-b0[0] * L2E), v0[1] * __builtin_amdgcn_exp2f(-b0[1] * L2E));
;                             o[1] = cvt_pk_bf16(v0[2] * __builtin_amdgcn_exp2f(-b0[2] * L2E), v0[3] * __builtin_amdgcn_exp2f(-b0[3] * L2E));
.LBB0_389:
	v_mul_f32_e32 v128, s10, v131
	v_exp_f32_e32 v130, v128
	v_mov_b32_e32 v153, v169
	v_mov_b32_e32 v149, v169
	v_lshl_add_u64 v[128:129], s[42:43], 0, v[152:153]
	v_mul_f32_e32 v130, v157, v130
	v_cvt_pk_bf16_f32 v147, v156, v130
	v_lshl_add_u64 v[128:129], v[128:129], 0, v[148:149]
	global_store_dwordx4 v[128:129], v[144:147], off nt
	s_waitcnt vmcnt(10)
	v_mov_b32_e32 v128, v230
	v_mov_b32_e32 v129, v231
	v_mov_b32_e32 v130, v232
	v_mov_b32_e32 v131, v233
	v_mov_b32_e32 v136, v234
	v_mov_b32_e32 v137, v235
	v_mov_b32_e32 v138, v236
	v_mov_b32_e32 v139, v237
	s_mov_b32 s100, 0x50000
	s_mov_b32 s101, 0
	v_lshl_add_u64 v[204:205], v[206:207], 0, s[100:101]
	global_load_dwordx4 v[230:233], v[204:205], off offset:528
	global_load_dwordx4 v[234:237], v[204:205], off offset:512
	s_nop 0
	s_and_b64 vcc, exec, s[8:9]
	s_mov_b64 s[10:11], -1
	s_cbranch_vccnz .LBB0_391
	v_mul_f32_e32 v144, 0xbfb8aa3b, v140
	v_mul_f32_e32 v145, 0xbfb8aa3b, v141
	v_exp_f32_e32 v144, v144
	v_exp_f32_e32 v145, v145
	s_mov_b64 s[10:11], 0
	v_mov_b32_e32 v153, v59
	v_pk_mul_f32 v[144:145], v[60:61], v[144:145]
	s_nop 0
	v_cvt_pk_bf16_f32 v144, v144, v145
	v_mul_f32_e32 v145, 0xbfb8aa3b, v142
	v_exp_f32_e32 v146, v145
	v_mul_f32_e32 v145, 0xbfb8aa3b, v143
	v_exp_f32_e32 v147, v145
	s_nop 0
	v_pk_mul_f32 v[146:147], v[62:63], v[146:147]
	s_nop 0
	v_cvt_pk_bf16_f32 v145, v146, v147
	v_mul_f32_e32 v146, 0xbfb8aa3b, v132
	v_mul_f32_e32 v147, 0xbfb8aa3b, v133
	v_exp_f32_e32 v146, v146
	v_exp_f32_e32 v147, v147
	s_nop 0
	v_pk_mul_f32 v[146:147], v[56:57], v[146:147]
	s_nop 0
	v_cvt_pk_bf16_f32 v146, v146, v147
	v_mul_f32_e32 v147, 0xbfb8aa3b, v134
	v_exp_f32_e32 v147, v147
	s_nop 0
	v_mul_f32_e32 v152, v58, v147
.LBB0_391:
	s_andn2_b64 vcc, exec, s[10:11]
	s_mov_b32 s10, 0xbfb8aa3b
	s_cbranch_vccnz .LBB0_393
	v_mul_f32_e32 v140, 0x3fb8aa3b, v140
	v_mul_f32_e32 v141, 0x3fb8aa3b, v141
	v_exp_f32_e32 v140, v140
	v_exp_f32_e32 v141, v141
	v_pk_mul_f32 v[144:145], v[60:61], s[34:35] op_sel_hi:[1,0]
	v_mul_f32_e32 v132, 0x3fb8aa3b, v132
	v_mul_f32_e32 v133, 0x3fb8aa3b, v133
	v_pk_mul_f32 v[140:141], v[144:145], v[140:141]
	v_exp_f32_e32 v132, v132
	v_cvt_pk_bf16_f32 v144, v140, v141
	v_mul_f32_e32 v140, 0x3fb8aa3b, v142
	v_mul_f32_e32 v141, 0x3fb8aa3b, v143
	v_exp_f32_e32 v140, v140
	v_exp_f32_e32 v141, v141
	v_exp_f32_e32 v133, v133
	v_pk_mul_f32 v[142:143], v[62:63], s[34:35] op_sel_hi:[1,0]
	s_mov_b32 s10, 0x3fb8aa3b
	v_pk_mul_f32 v[140:141], v[142:143], v[140:141]
	s_nop 0
	v_cvt_pk_bf16_f32 v145, v140, v141
	v_pk_mul_f32 v[140:141], v[56:57], s[34:35] op_sel_hi:[1,0]
	s_nop 0
	v_pk_mul_f32 v[132:133], v[140:141], v[132:133]
	s_nop 0
	v_cvt_pk_bf16_f32 v146, v132, v133
	v_mul_f32_e32 v133, 0x3fb8aa3b, v134
	v_exp_f32_e32 v190, v133
	v_mul_f32_e32 v132, 0x3db504f3, v58
	v_mov_b32_e32 v133, v59
	v_pk_mul_f32 v[152:153], v[132:133], v[190:191]
.LBB0_393:
	v_mul_f32_e32 v133, s10, v135
	v_ashrrev_i32_e32 v132, 9, v150
	v_exp_f32_e32 v134, v133
	v_and_b32_e32 v151, -4, v132
	v_add_u32_e32 v132, s17, v151
	v_ashrrev_i32_e32 v133, 31, v132
	v_lshlrev_b32_e32 v135, 7, v150
	v_and_b32_e32 v193, 0x3e780, v135
	v_mul_f32_e32 v134, v153, v134
	v_lshlrev_b64 v[132:133], 19, v[132:133]
	v_cvt_pk_bf16_f32 v147, v152, v134
	v_lshl_add_u64 v[152:153], s[2:3], 0, v[132:133]
	v_lshlrev_b32_e32 v156, 1, v193
	v_mov_b32_e32 v157, v169
	v_lshl_add_u64 v[132:133], v[152:153], 0, v[156:157]
	v_mov_b32_e32 v149, v169
	v_lshl_add_u64 v[132:133], v[132:133], 0, v[148:149]
	global_store_dwordx4 v[132:133], v[144:147], off nt
	v_or_b32_e32 v132, 16, v150
	v_ashrrev_i32_e32 v133, 31, v132
	v_lshlrev_b64 v[132:133], 11, v[132:133]
	v_lshl_add_u64 v[132:133], s[22:23], 0, v[132:133]
	v_lshl_add_u64 v[158:159], v[168:169], 2, v[132:133]
	s_waitcnt vmcnt(10)
	v_mov_b32_e32 v132, v196
	v_mov_b32_e32 v133, v197
	v_mov_b32_e32 v134, v198
	v_mov_b32_e32 v135, v199
	v_mov_b32_e32 v140, v200
	v_mov_b32_e32 v141, v201
	v_mov_b32_e32 v142, v202
	v_mov_b32_e32 v143, v203
	s_mov_b32 s100, 0x58000
	s_mov_b32 s101, 0
	v_lshl_add_u64 v[204:205], v[206:207], 0, s[100:101]
	global_load_dwordx4 v[196:199], v[204:205], off offset:16
	global_load_dwordx4 v[200:203], v[204:205], off
	s_and_b64 vcc, exec, s[8:9]
	s_mov_b64 s[10:11], -1
	s_cbranch_vccnz .LBB0_395
	v_mul_f32_e32 v144, 0xbfb8aa3b, v136
	v_mul_f32_e32 v145, 0xbfb8aa3b, v137
	v_exp_f32_e32 v144, v144
	v_exp_f32_e32 v145, v145
	s_mov_b64 s[10:11], 0
	v_mov_b32_e32 v155, v51
	v_pk_mul_f32 v[144:145], v[52:53], v[144:145]
	s_nop 0
	v_cvt_pk_bf16_f32 v144, v144, v145
	v_mul_f32_e32 v145, 0xbfb8aa3b, v138
	v_exp_f32_e32 v146, v145
	v_mul_f32_e32 v145, 0xbfb8aa3b, v139
	v_exp_f32_e32 v147, v145
	s_nop 0
	v_pk_mul_f32 v[146:147], v[54:55], v[146:147]
	s_nop 0
	v_cvt_pk_bf16_f32 v145, v146, v147
	v_mul_f32_e32 v146, 0xbfb8aa3b, v128
	v_mul_f32_e32 v147, 0xbfb8aa3b, v129
	v_exp_f32_e32 v146, v146
	v_exp_f32_e32 v147, v147
	s_nop 0
	v_pk_mul_f32 v[146:147], v[48:49], v[146:147]
	s_nop 0
	v_cvt_pk_bf16_f32 v146, v146, v147
	v_mul_f32_e32 v147, 0xbfb8aa3b, v130
	v_exp_f32_e32 v147, v147
	s_nop 0
	v_mul_f32_e32 v154, v50, v147

;     __device__ __forceinline__ void operator()(const f32x4 (&acc)[2][2][4][2], const Unit& u, int wr, int wc, int fr, int fq) const {
;     ...
;         } else if (u.pn < 16) {
;             const bool isq = u.pn < 14;
;             const int cb = (u.pn - (isq ? 12 : 14)) * 256;
;             bf16_t* d0 = (bf16_t*)(ws + (isq ? WS_QG : WS_KG));
;             f32x4 bc[2][2];
;     ...
;             BC_LOAD(0, 0);
; #pragma unroll
;             for (int g = 0; g < 16; ++g) {
;                 const int ai = g >> 3, m = (g >> 1) & 3, bj = g & 1;
;                 const int r = row0 + ai * HALF + m * 16;
;                 if (g + 1 < 16) BC_LOAD((g + 1) & 1, g + 1);
;                 {
;                     {
;                         const int col = cb + bj * HALF + lc;
;                         const size_t hoff = ((size_t)((r >> 11) * 4 + (col >> 7)) * SEQ + (r & (SEQ - 1))) * 128 + (col & 127);
;                         const f32x4 b0 = bc[g & 1][0], b1 = bc[g & 1][1];
;                         const f32x4 v0 = acc[ai][bj][m][0], v1 = acc[ai][bj][m][1];
;                         const float L2E = 1.4426950408889634f;
;                         if (isq) {
;                             const float s = 0.08838834764831845f;
;                             u32x4 o; o[0] = cvt_pk_bf16(v0[0] * s * __builtin_amdgcn_exp2f(b0[0] * L2E), v0[1] * s * __builtin_amdgcn_exp2f(b0[1] * L2E));
;                             o[1] = cvt_pk_bf16(v0[2] * s * __builtin_amdgcn_exp2f(b0[2] * L2E), v0[3] * s * __builtin_amdgcn_exp2f(b0[3] * L2E));
;                             o[2] = cvt_pk_bf16(v1[0] * s * __builtin_amdgcn_exp2f(b1[0] * L2E), v1[1] * s * __builtin_amdgcn_exp2f(b1[1] * L2E));
;                             o[3] = cvt_pk_bf16(v1[2] * s * __builtin_amdgcn_exp2f(b1[2] * L2E), v1[3] * s * __builtin_amdgcn_exp2f(b1[3] * L2E));
;                             __builtin_nontemporal_store(o, (u32x4*)(d0 + hoff));
;                         } else {
;                             u32x4 o;
;                             o[0] = cvt_pk_bf16(v0[0] * __builtin_amdgcn_exp2f(-b0[0] * L2E), v0[1] * __builtin_amdgcn_exp2f(-b0[1] * L2E));
;                             o[1] = cvt_pk_bf16(v0[2] * __builtin_amdgcn_exp2f(-b0[2] * L2E), v0[3] * __builtin_amdgcn_exp2f(-b0[3] * L2E));
.LBB0_397:
	v_mul_f32_e32 v128, s10, v131
	v_exp_f32_e32 v130, v128
	v_add_u32_e32 v128, s18, v151
	v_ashrrev_i32_e32 v129, 31, v128
	v_lshlrev_b64 v[128:129], 19, v[128:129]
	v_mul_f32_e32 v130, v155, v130
	v_cvt_pk_bf16_f32 v147, v154, v130
	v_lshl_add_u64 v[154:155], s[2:3], 0, v[128:129]
	v_mov_b32_e32 v157, v169
	v_lshl_add_u64 v[128:129], v[154:155], 0, v[156:157]
	v_mov_b32_e32 v149, v169
	v_lshl_add_u64 v[128:129], v[128:129], 0, v[148:149]
	global_store_dwordx4 v[128:129], v[144:147], off nt
	s_waitcnt vmcnt(10)
	v_mov_b32_e32 v128, v214
	v_mov_b32_e32 v129, v215
	v_mov_b32_e32 v130, v216
	v_mov_b32_e32 v131, v217
	v_mov_b32_e32 v136, v218
	v_mov_b32_e32 v137, v219
	v_mov_b32_e32 v138, v220
	v_mov_b32_e32 v139, v221
	s_mov_b32 s100, 0x58000
	s_mov_b32 s101, 0
	v_lshl_add_u64 v[204:205], v[206:207], 0, s[100:101]
	global_load_dwordx4 v[214:217], v[204:205], off offset:528
	global_load_dwordx4 v[218:221], v[204:205], off offset:512
	s_nop 0
	s_and_b64 vcc, exec, s[8:9]
	s_mov_b64 s[2:3], -1
	s_cbranch_vccnz .LBB0_399
	v_mul_f32_e32 v144, 0xbfb8aa3b, v140
	v_mul_f32_e32 v145, 0xbfb8aa3b, v141
	v_exp_f32_e32 v144, v144
	v_exp_f32_e32 v145, v145
	s_mov_b64 s[2:3], 0
	v_mov_b32_e32 v159, v43
	v_pk_mul_f32 v[144:145], v[44:45], v[144:145]
	s_nop 0
	v_cvt_pk_bf16_f32 v144, v144, v145
	v_mul_f32_e32 v145, 0xbfb8aa3b, v142
	v_exp_f32_e32 v146, v145
	v_mul_f32_e32 v145, 0xbfb8aa3b, v143
	v_exp_f32_e32 v147, v145
	s_nop 0
	v_pk_mul_f32 v[146:147], v[46:47], v[146:147]
	s_nop 0
	v_cvt_pk_bf16_f32 v145, v146, v147
	v_mul_f32_e32 v146, 0xbfb8aa3b, v132
	v_mul_f32_e32 v147, 0xbfb8aa3b, v133
	v_exp_f32_e32 v146, v146
	v_exp_f32_e32 v147, v147
	s_nop 0
	v_pk_mul_f32 v[146:147], v[40:41], v[146:147]
	s_nop 0
	v_cvt_pk_bf16_f32 v146, v146, v147
	v_mul_f32_e32 v147, 0xbfb8aa3b, v134
	v_exp_f32_e32 v147, v147
	s_nop 0
	v_mul_f32_e32 v158, v42, v147
.LBB0_399:
	s_andn2_b64 vcc, exec, s[2:3]
	s_mov_b32 s2, 0xbfb8aa3b
	s_cbranch_vccnz .LBB0_401
	v_mul_f32_e32 v140, 0x3fb8aa3b, v140
	v_mul_f32_e32 v141, 0x3fb8aa3b, v141
	v_exp_f32_e32 v140, v140
	v_exp_f32_e32 v141, v141
	v_pk_mul_f32 v[144:145], v[44:45], s[34:35] op_sel_hi:[1,0]
	v_mul_f32_e32 v132, 0x3fb8aa3b, v132
	v_mul_f32_e32 v133, 0x3fb8aa3b, v133
	v_pk_mul_f32 v[140:141], v[144:145], v[140:141]
	v_exp_f32_e32 v132, v132
	v_cvt_pk_bf16_f32 v144, v140, v141
	v_mul_f32_e32 v140, 0x3fb8aa3b, v142
	v_mul_f32_e32 v141, 0x3fb8aa3b, v143
	v_exp_f32_e32 v140, v140
	v_exp_f32_e32 v141, v141
	v_exp_f32_e32 v133, v133
	v_pk_mul_f32 v[142:143], v[46:47], s[34:35] op_sel_hi:[1,0]
	v_mul_f32_e32 v134, 0x3fb8aa3b, v134
	v_pk_mul_f32 v[140:141], v[142:143], v[140:141]
	v_exp_f32_e32 v190, v134
	v_cvt_pk_bf16_f32 v145, v140, v141
	v_pk_mul_f32 v[140:141], v[40:41], s[34:35] op_sel_hi:[1,0]
	s_mov_b32 s2, 0x3fb8aa3b
	v_pk_mul_f32 v[132:133], v[140:141], v[132:133]
	s_nop 0
	v_cvt_pk_bf16_f32 v146, v132, v133
	v_mul_f32_e32 v132, 0x3db504f3, v42
	v_mov_b32_e32 v133, v43
	v_pk_mul_f32 v[158:159], v[132:133], v[190:191]
.LBB0_401:
	v_mul_f32_e32 v132, s2, v135
	v_exp_f32_e32 v132, v132
	v_or_b32_e32 v133, 0x800, v193
	v_mov_b32_e32 v157, v169
	v_lshlrev_b32_e32 v156, 1, v133
	v_mul_f32_e32 v132, v159, v132
	v_cvt_pk_bf16_f32 v147, v158, v132
	v_lshl_add_u64 v[132:133], v[152:153], 0, v[156:157]
	v_mov_b32_e32 v149, v169
	v_lshl_add_u64 v[132:133], v[132:133], 0, v[148:149]
	global_store_dwordx4 v[132:133], v[144:147], off nt
	v_or_b32_e32 v132, 32, v150
	v_ashrrev_i32_e32 v133, 31, v132
	v_lshlrev_b64 v[132:133], 11, v[132:133]
	v_lshl_add_u64 v[132:133], s[22:23], 0, v[132:133]
	v_lshl_add_u64 v[158:159], v[168:169], 2, v[132:133]
	s_waitcnt vmcnt(10)
	v_mov_b32_e32 v132, v222
	v_mov_b32_e32 v133, v223
	v_mov_b32_e32 v134, v224
	v_mov_b32_e32 v135, v225
	v_mov_b32_e32 v140, v226
	v_mov_b32_e32 v141, v227
	v_mov_b32_e32 v142, v228
	v_mov_b32_e32 v143, v229
	s_and_b64 vcc, exec, s[8:9]
	s_mov_b64 s[2:3], -1
	s_cbranch_vccnz .LBB0_403
	v_mul_f32_e32 v144, 0xbfb8aa3b, v136
	v_mul_f32_e32 v145, 0xbfb8aa3b, v137
	v_exp_f32_e32 v144, v144
	v_exp_f32_e32 v145, v145
	s_mov_b64 s[2:3], 0
	v_mov_b32_e32 v195, v35
	v_pk_mul_f32 v[144:145], v[36:37], v[144:145]
	s_nop 0
	v_cvt_pk_bf16_f32 v144, v144, v145
	v_mul_f32_e32 v145, 0xbfb8aa3b, v138
	v_exp_f32_e32 v146, v145
	v_mul_f32_e32 v145, 0xbfb8aa3b, v139
	v_exp_f32_e32 v147, v145
	s_nop 0
	v_pk_mul_f32 v[146:147], v[38:39], v[146:147]
	s_nop 0
	v_cvt_pk_bf16_f32 v145, v146, v147
	v_mul_f32_e32 v146, 0xbfb8aa3b, v128
	v_mul_f32_e32 v147, 0xbfb8aa3b, v129
	v_exp_f32_e32 v146, v146
	v_exp_f32_e32 v147, v147
	s_nop 0
	v_pk_mul_f32 v[146:147], v[32:33], v[146:147]
	s_nop 0
	v_cvt_pk_bf16_f32 v146, v146, v147
	v_mul_f32_e32 v147, 0xbfb8aa3b, v130
	v_exp_f32_e32 v147, v147
	s_nop 0
	v_mul_f32_e32 v194, v34, v147

;     __device__ __forceinline__ void operator()(const f32x4 (&acc)[2][2][4][2], const Unit& u, int wr, int wc, int fr, int fq) const {
;     ...
;         } else if (u.pn < 16) {
;             const bool isq = u.pn < 14;
;             const int cb = (u.pn - (isq ? 12 : 14)) * 256;
;             bf16_t* d0 = (bf16_t*)(ws + (isq ? WS_QG : WS_KG));
;             f32x4 bc[2][2];
;     ...
;             BC_LOAD(0, 0);
; #pragma unroll
;             for (int g = 0; g < 16; ++g) {
;                 const int ai = g >> 3, m = (g >> 1) & 3, bj = g & 1;
;                 const int r = row0 + ai * HALF + m * 16;
;                 if (g + 1 < 16) BC_LOAD((g + 1) & 1, g + 1);
;                 {
;                     {
;                         const int col = cb + bj * HALF + lc;
;                         const size_t hoff = ((size_t)((r >> 11) * 4 + (col >> 7)) * SEQ + (r & (SEQ - 1))) * 128 + (col & 127);
;                         const f32x4 b0 = bc[g & 1][0], b1 = bc[g & 1][1];
;                         const f32x4 v0 = acc[ai][bj][m][0], v1 = acc[ai][bj][m][1];
;                         const float L2E = 1.4426950408889634f;
;                         if (isq) {
;                             const float s = 0.08838834764831845f;
;                             u32x4 o; o[0] = cvt_pk_bf16(v0[0] * s * __builtin_amdgcn_exp2f(b0[0] * L2E), v0[1] * s * __builtin_amdgcn_exp2f(b0[1] * L2E));
;                             o[1] = cvt_pk_bf16(v0[2] * s * __builtin_amdgcn_exp2f(b0[2] * L2E), v0[3] * s * __builtin_amdgcn_exp2f(b0[3] * L2E));
;                             o[2] = cvt_pk_bf16(v1[0] * s * __builtin_amdgcn_exp2f(b1[0] * L2E), v1[1] * s * __builtin_amdgcn_exp2f(b1[1] * L2E));
;                             o[3] = cvt_pk_bf16(v1[2] * s * __builtin_amdgcn_exp2f(b1[2] * L2E), v1[3] * s * __builtin_amdgcn_exp2f(b1[3] * L2E));
;                             __builtin_nontemporal_store(o, (u32x4*)(d0 + hoff));
;                         } else {
;                             u32x4 o;
;                             o[0] = cvt_pk_bf16(v0[0] * __builtin_amdgcn_exp2f(-b0[0] * L2E), v0[1] * __builtin_amdgcn_exp2f(-b0[1] * L2E));
;                             o[1] = cvt_pk_bf16(v0[2] * __builtin_amdgcn_exp2f(-b0[2] * L2E), v0[3] * __builtin_amdgcn_exp2f(-b0[3] * L2E));
.LBB0_405:
	v_mul_f32_e32 v128, s2, v131
	v_exp_f32_e32 v130, v128
	v_mov_b32_e32 v157, v169
	v_mov_b32_e32 v149, v169
	v_lshl_add_u64 v[128:129], v[154:155], 0, v[156:157]
	v_mul_f32_e32 v130, v195, v130
	v_cvt_pk_bf16_f32 v147, v194, v130
	v_lshl_add_u64 v[128:129], v[128:129], 0, v[148:149]
	global_store_dwordx4 v[128:129], v[144:147], off nt
	s_waitcnt vmcnt(8)
	v_mov_b32_e32 v128, v230
	v_mov_b32_e32 v129, v231
	v_mov_b32_e32 v130, v232
	v_mov_b32_e32 v131, v233
	v_mov_b32_e32 v136, v234
	v_mov_b32_e32 v137, v235
	v_mov_b32_e32 v138, v236
	v_mov_b32_e32 v139, v237
	s_nop 0
	s_and_b64 vcc, exec, s[8:9]
	s_mov_b64 s[2:3], -1
	s_cbranch_vccnz .LBB0_407
	v_mul_f32_e32 v144, 0xbfb8aa3b, v140
	v_mul_f32_e32 v145, 0xbfb8aa3b, v141
	v_exp_f32_e32 v144, v144
	v_exp_f32_e32 v145, v145
	s_mov_b64 s[2:3], 0
	v_mov_b32_e32 v159, v27
	v_pk_mul_f32 v[144:145], v[28:29], v[144:145]
	s_nop 0
	v_cvt_pk_bf16_f32 v144, v144, v145
	v_mul_f32_e32 v145, 0xbfb8aa3b, v142
	v_exp_f32_e32 v146, v145
	v_mul_f32_e32 v145, 0xbfb8aa3b, v143
	v_exp_f32_e32 v147, v145
	s_nop 0
	v_pk_mul_f32 v[146:147], v[30:31], v[146:147]
	s_nop 0
	v_cvt_pk_bf16_f32 v145, v146, v147
	v_mul_f32_e32 v146, 0xbfb8aa3b, v132
	v_mul_f32_e32 v147, 0xbfb8aa3b, v133
	v_exp_f32_e32 v146, v146
	v_exp_f32_e32 v147, v147
	s_nop 0
	v_pk_mul_f32 v[146:147], v[24:25], v[146:147]
	s_nop 0
	v_cvt_pk_bf16_f32 v146, v146, v147
	v_mul_f32_e32 v147, 0xbfb8aa3b, v134
	v_exp_f32_e32 v147, v147
	s_nop 0
	v_mul_f32_e32 v158, v26, v147
.LBB0_407:
	s_andn2_b64 vcc, exec, s[2:3]
	s_mov_b32 s2, 0xbfb8aa3b
	s_cbranch_vccnz .LBB0_409
	v_mul_f32_e32 v140, 0x3fb8aa3b, v140
	v_mul_f32_e32 v141, 0x3fb8aa3b, v141
	v_exp_f32_e32 v140, v140
	v_exp_f32_e32 v141, v141
	v_pk_mul_f32 v[144:145], v[28:29], s[34:35] op_sel_hi:[1,0]
	v_mul_f32_e32 v132, 0x3fb8aa3b, v132
	v_mul_f32_e32 v133, 0x3fb8aa3b, v133
	v_pk_mul_f32 v[140:141], v[144:145], v[140:141]
	v_exp_f32_e32 v132, v132
	v_cvt_pk_bf16_f32 v144, v140, v141
	v_mul_f32_e32 v140, 0x3fb8aa3b, v142
	v_mul_f32_e32 v141, 0x3fb8aa3b, v143
	v_exp_f32_e32 v140, v140
	v_exp_f32_e32 v141, v141
	v_exp_f32_e32 v133, v133
	v_pk_mul_f32 v[142:143], v[30:31], s[34:35] op_sel_hi:[1,0]
	v_mul_f32_e32 v134, 0x3fb8aa3b, v134
	v_pk_mul_f32 v[140:141], v[142:143], v[140:141]
	v_exp_f32_e32 v190, v134
	v_cvt_pk_bf16_f32 v145, v140, v141
	v_pk_mul_f32 v[140:141], v[24:25], s[34:35] op_sel_hi:[1,0]
	s_mov_b32 s2, 0x3fb8aa3b
	v_pk_mul_f32 v[132:133], v[140:141], v[132:133]
	s_nop 0
	v_cvt_pk_bf16_f32 v146, v132, v133
	v_mul_f32_e32 v132, 0x3db504f3, v26
	v_mov_b32_e32 v133, v27
	v_pk_mul_f32 v[158:159], v[132:133], v[190:191]
.LBB0_409:
	v_mul_f32_e32 v132, s2, v135
	v_exp_f32_e32 v132, v132
	v_or_b32_e32 v133, 0x1000, v193
	v_mov_b32_e32 v157, v169
	v_lshlrev_b32_e32 v156, 1, v133
	v_mul_f32_e32 v132, v159, v132
	v_cvt_pk_bf16_f32 v147, v158, v132
	v_lshl_add_u64 v[132:133], v[152:153], 0, v[156:157]
	v_mov_b32_e32 v149, v169
	v_lshl_add_u64 v[132:133], v[132:133], 0, v[148:149]
	global_store_dwordx4 v[132:133], v[144:147], off nt
	v_or_b32_e32 v132, 48, v150
	v_ashrrev_i32_e32 v133, 31, v132
	v_lshlrev_b64 v[132:133], 11, v[132:133]
	v_lshl_add_u64 v[132:133], s[22:23], 0, v[132:133]
	v_lshl_add_u64 v[150:151], v[168:169], 2, v[132:133]
	s_waitcnt vmcnt(6)
	v_mov_b32_e32 v132, v196
	v_mov_b32_e32 v133, v197
	v_mov_b32_e32 v134, v198
	v_mov_b32_e32 v135, v199
	v_mov_b32_e32 v140, v200
	v_mov_b32_e32 v141, v201
	v_mov_b32_e32 v142, v202
	v_mov_b32_e32 v143, v203
	s_and_b64 vcc, exec, s[8:9]
	s_mov_b64 s[2:3], -1
	s_cbranch_vccnz .LBB0_411
	v_mul_f32_e32 v144, 0xbfb8aa3b, v136
	v_mul_f32_e32 v145, 0xbfb8aa3b, v137
	v_exp_f32_e32 v144, v144
	v_exp_f32_e32 v145, v145
	s_mov_b64 s[2:3], 0
	v_mov_b32_e32 v159, v19
	v_pk_mul_f32 v[144:145], v[20:21], v[144:145]
	s_nop 0
	v_cvt_pk_bf16_f32 v144, v144, v145
	v_mul_f32_e32 v145, 0xbfb8aa3b, v138
	v_exp_f32_e32 v146, v145
	v_mul_f32_e32 v145, 0xbfb8aa3b, v139
	v_exp_f32_e32 v147, v145
	s_nop 0
	v_pk_mul_f32 v[146:147], v[22:23], v[146:147]
	s_nop 0
	v_cvt_pk_bf16_f32 v145, v146, v147
	v_mul_f32_e32 v146, 0xbfb8aa3b, v128
	v_mul_f32_e32 v147, 0xbfb8aa3b, v129
	v_exp_f32_e32 v146, v146
	v_exp_f32_e32 v147, v147
	s_nop 0
	v_pk_mul_f32 v[146:147], v[16:17], v[146:147]
	s_nop 0
	v_cvt_pk_bf16_f32 v146, v146, v147
	v_mul_f32_e32 v147, 0xbfb8aa3b, v130
	v_exp_f32_e32 v147, v147
	s_nop 0
	v_mul_f32_e32 v158, v18, v147

;     __device__ __forceinline__ void operator()(const f32x4 (&acc)[2][2][4][2], const Unit& u, int wr, int wc, int fr, int fq) const {
;     ...
;         } else if (u.pn < 16) {
;             const bool isq = u.pn < 14;
;             const int cb = (u.pn - (isq ? 12 : 14)) * 256;
;             bf16_t* d0 = (bf16_t*)(ws + (isq ? WS_QG : WS_KG));
;             f32x4 bc[2][2];
;     ...
;             BC_LOAD(0, 0);
; #pragma unroll
;             for (int g = 0; g < 16; ++g) {
;                 const int ai = g >> 3, m = (g >> 1) & 3, bj = g & 1;
;                 const int r = row0 + ai * HALF + m * 16;
;                 if (g + 1 < 16) BC_LOAD((g + 1) & 1, g + 1);
;                 {
;                     {
;                         const int col = cb + bj * HALF + lc;
;                         const size_t hoff = ((size_t)((r >> 11) * 4 + (col >> 7)) * SEQ + (r & (SEQ - 1))) * 128 + (col & 127);
;                         const f32x4 b0 = bc[g & 1][0], b1 = bc[g & 1][1];
;                         const f32x4 v0 = acc[ai][bj][m][0], v1 = acc[ai][bj][m][1];
;                         const float L2E = 1.4426950408889634f;
;                         if (isq) {
;                             const float s = 0.08838834764831845f;
;                             u32x4 o; o[0] = cvt_pk_bf16(v0[0] * s * __builtin_amdgcn_exp2f(b0[0] * L2E), v0[1] * s * __builtin_amdgcn_exp2f(b0[1] * L2E));
;                             o[1] = cvt_pk_bf16(v0[2] * s * __builtin_amdgcn_exp2f(b0[2] * L2E), v0[3] * s * __builtin_amdgcn_exp2f(b0[3] * L2E));
;                             o[2] = cvt_pk_bf16(v1[0] * s * __builtin_amdgcn_exp2f(b1[0] * L2E), v1[1] * s * __builtin_amdgcn_exp2f(b1[1] * L2E));
;                             o[3] = cvt_pk_bf16(v1[2] * s * __builtin_amdgcn_exp2f(b1[2] * L2E), v1[3] * s * __builtin_amdgcn_exp2f(b1[3] * L2E));
;                             __builtin_nontemporal_store(o, (u32x4*)(d0 + hoff));
;                         } else {
;                             u32x4 o;
;                             o[0] = cvt_pk_bf16(v0[0] * __builtin_amdgcn_exp2f(-b0[0] * L2E), v0[1] * __builtin_amdgcn_exp2f(-b0[1] * L2E));
;                             o[1] = cvt_pk_bf16(v0[2] * __builtin_amdgcn_exp2f(-b0[2] * L2E), v0[3] * __builtin_amdgcn_exp2f(-b0[3] * L2E));
.LBB0_413:
	v_mul_f32_e32 v128, s2, v131
	v_exp_f32_e32 v130, v128
	v_mov_b32_e32 v157, v169
	v_mov_b32_e32 v149, v169
	v_lshl_add_u64 v[128:129], v[154:155], 0, v[156:157]
	v_mul_f32_e32 v130, v159, v130
	v_cvt_pk_bf16_f32 v147, v158, v130
	v_lshl_add_u64 v[128:129], v[128:129], 0, v[148:149]
	global_store_dwordx4 v[128:129], v[144:147], off nt
	s_waitcnt vmcnt(4)
	v_mov_b32_e32 v128, v214
	v_mov_b32_e32 v129, v215
	v_mov_b32_e32 v130, v216
	v_mov_b32_e32 v131, v217
	v_mov_b32_e32 v136, v218
	v_mov_b32_e32 v137, v219
	v_mov_b32_e32 v138, v220
	v_mov_b32_e32 v139, v221
	s_nop 0
	s_and_b64 vcc, exec, s[8:9]
	s_mov_b64 s[2:3], -1
	s_cbranch_vccnz .LBB0_415
	v_mul_f32_e32 v144, 0xbfb8aa3b, v140
	v_mul_f32_e32 v145, 0xbfb8aa3b, v141
	v_exp_f32_e32 v144, v144
	v_exp_f32_e32 v145, v145
	s_mov_b64 s[2:3], 0
	v_mov_b32_e32 v151, v11
	v_pk_mul_f32 v[144:145], v[12:13], v[144:145]
	s_nop 0
	v_cvt_pk_bf16_f32 v144, v144, v145
	v_mul_f32_e32 v145, 0xbfb8aa3b, v142
	v_exp_f32_e32 v146, v145
	v_mul_f32_e32 v145, 0xbfb8aa3b, v143
	v_exp_f32_e32 v147, v145
	s_nop 0
	v_pk_mul_f32 v[146:147], v[14:15], v[146:147]
	s_nop 0
	v_cvt_pk_bf16_f32 v145, v146, v147
	v_mul_f32_e32 v146, 0xbfb8aa3b, v132
	v_mul_f32_e32 v147, 0xbfb8aa3b, v133
	v_exp_f32_e32 v146, v146
	v_exp_f32_e32 v147, v147
	s_nop 0
	v_pk_mul_f32 v[146:147], v[8:9], v[146:147]
	s_nop 0
	v_cvt_pk_bf16_f32 v146, v146, v147
	v_mul_f32_e32 v147, 0xbfb8aa3b, v134
	v_exp_f32_e32 v147, v147
	s_nop 0
	v_mul_f32_e32 v150, v10, v147
.LBB0_415:
	s_andn2_b64 vcc, exec, s[2:3]
	s_mov_b32 s2, 0xbfb8aa3b
	s_cbranch_vccnz .LBB0_417
	v_mul_f32_e32 v140, 0x3fb8aa3b, v140
	v_mul_f32_e32 v141, 0x3fb8aa3b, v141
	v_exp_f32_e32 v140, v140
	v_exp_f32_e32 v141, v141
	v_pk_mul_f32 v[144:145], v[12:13], s[34:35] op_sel_hi:[1,0]
	v_mul_f32_e32 v132, 0x3fb8aa3b, v132
	v_mul_f32_e32 v133, 0x3fb8aa3b, v133
	v_pk_mul_f32 v[140:141], v[144:145], v[140:141]
	v_exp_f32_e32 v132, v132
	v_cvt_pk_bf16_f32 v144, v140, v141
	v_mul_f32_e32 v140, 0x3fb8aa3b, v142
	v_mul_f32_e32 v141, 0x3fb8aa3b, v143
	v_exp_f32_e32 v140, v140
	v_exp_f32_e32 v141, v141
	v_exp_f32_e32 v133, v133
	v_pk_mul_f32 v[142:143], v[14:15], s[34:35] op_sel_hi:[1,0]
	v_mul_f32_e32 v134, 0x3fb8aa3b, v134
	v_pk_mul_f32 v[140:141], v[142:143], v[140:141]
	v_exp_f32_e32 v190, v134
	v_cvt_pk_bf16_f32 v145, v140, v141
	v_pk_mul_f32 v[140:141], v[8:9], s[34:35] op_sel_hi:[1,0]
	s_mov_b32 s2, 0x3fb8aa3b
	v_pk_mul_f32 v[132:133], v[140:141], v[132:133]
	s_nop 0
	v_cvt_pk_bf16_f32 v146, v132, v133
	v_mul_f32_e32 v132, 0x3db504f3, v10
	v_mov_b32_e32 v133, v11
	v_pk_mul_f32 v[150:151], v[132:133], v[190:191]
.LBB0_417:
	v_mul_f32_e32 v132, s2, v135
	v_exp_f32_e32 v134, v132
	v_or_b32_e32 v132, 0x1800, v193
	v_lshlrev_b32_e32 v168, 1, v132
	v_lshl_add_u64 v[132:133], v[152:153], 0, v[168:169]
	v_mul_f32_e32 v134, v151, v134
	v_mov_b32_e32 v149, v169
	v_cvt_pk_bf16_f32 v147, v150, v134
	v_lshl_add_u64 v[132:133], v[132:133], 0, v[148:149]
	s_and_b64 vcc, exec, s[8:9]
	s_mov_b64 s[2:3], -1
	global_store_dwordx4 v[132:133], v[144:147], off nt
	s_cbranch_vccnz .LBB0_419
	v_mul_f32_e32 v132, 0xbfb8aa3b, v136
	v_mul_f32_e32 v133, 0xbfb8aa3b, v137
	v_exp_f32_e32 v132, v132
	v_exp_f32_e32 v133, v133
	v_mul_f32_e32 v134, 0xbfb8aa3b, v138
	v_mul_f32_e32 v135, 0xbfb8aa3b, v139
	v_exp_f32_e32 v134, v134
	v_pk_mul_f32 v[132:133], v[4:5], v[132:133]
	v_exp_f32_e32 v135, v135
	v_cvt_pk_bf16_f32 v132, v132, v133
	v_mul_f32_e32 v133, 0xbfb8aa3b, v128
	v_exp_f32_e32 v140, v133
	v_mul_f32_e32 v133, 0xbfb8aa3b, v129
	v_exp_f32_e32 v141, v133
	v_mul_f32_e32 v133, 0xbfb8aa3b, v130
	v_exp_f32_e32 v142, v133
	v_pk_mul_f32 v[134:135], v[6:7], v[134:135]
	s_mov_b64 s[2:3], 0
	v_cvt_pk_bf16_f32 v133, v134, v135
	v_pk_mul_f32 v[134:135], v[0:1], v[140:141]
	v_mul_f32_e32 v140, v2, v142
	v_cvt_pk_bf16_f32 v134, v134, v135
	v_mov_b32_e32 v141, v3

;     __device__ __forceinline__ void operator()(const f32x4 (&acc)[2][2][4][2], const Unit& u, int wr, int wc, int fr, int fq) const {
;     ...
;         } else if (u.pn < 16) {
;             const bool isq = u.pn < 14;
;             const int cb = (u.pn - (isq ? 12 : 14)) * 256;
;             bf16_t* d0 = (bf16_t*)(ws + (isq ? WS_QG : WS_KG));
;             f32x4 bc[2][2];
;     ...
;             BC_LOAD(0, 0);
; #pragma unroll
;             for (int g = 0; g < 16; ++g) {
;                 const int ai = g >> 3, m = (g >> 1) & 3, bj = g & 1;
;                 const int r = row0 + ai * HALF + m * 16;
;                 if (g + 1 < 16) BC_LOAD((g + 1) & 1, g + 1);
;                 {
;                     {
;                         const int col = cb + bj * HALF + lc;
;                         const size_t hoff = ((size_t)((r >> 11) * 4 + (col >> 7)) * SEQ + (r & (SEQ - 1))) * 128 + (col & 127);
;                         const f32x4 b0 = bc[g & 1][0], b1 = bc[g & 1][1];
;                         const f32x4 v0 = acc[ai][bj][m][0], v1 = acc[ai][bj][m][1];
;                         const float L2E = 1.4426950408889634f;
;                         if (isq) {
;                             const float s = 0.08838834764831845f;
;                             u32x4 o; o[0] = cvt_pk_bf16(v0[0] * s * __builtin_amdgcn_exp2f(b0[0] * L2E), v0[1] * s * __builtin_amdgcn_exp2f(b0[1] * L2E));
;                             o[1] = cvt_pk_bf16(v0[2] * s * __builtin_amdgcn_exp2f(b0[2] * L2E), v0[3] * s * __builtin_amdgcn_exp2f(b0[3] * L2E));
;                             o[2] = cvt_pk_bf16(v1[0] * s * __builtin_amdgcn_exp2f(b1[0] * L2E), v1[1] * s * __builtin_amdgcn_exp2f(b1[1] * L2E));
;                             o[3] = cvt_pk_bf16(v1[2] * s * __builtin_amdgcn_exp2f(b1[2] * L2E), v1[3] * s * __builtin_amdgcn_exp2f(b1[3] * L2E));
;                             __builtin_nontemporal_store(o, (u32x4*)(d0 + hoff));
;                         } else {
;                             u32x4 o;
;                             o[0] = cvt_pk_bf16(v0[0] * __builtin_amdgcn_exp2f(-b0[0] * L2E), v0[1] * __builtin_amdgcn_exp2f(-b0[1] * L2E));
;                             o[1] = cvt_pk_bf16(v0[2] * __builtin_amdgcn_exp2f(-b0[2] * L2E), v0[3] * __builtin_amdgcn_exp2f(-b0[3] * L2E));
.LBB0_1413:
	s_and_b64 vcc, exec, s[2:3]
	s_cbranch_vccz .LBB0_1628
	s_cmp_gt_u32 s76, 13
	s_cselect_b64 s[42:43], -1, 0
	s_cmp_lt_u32 s76, 14
	s_cselect_b64 s[2:3], -1, 0
	s_and_b64 s[8:9], s[2:3], exec
	s_cselect_b32 s10, -12, -14
	v_ashrrev_i32_e32 v193, 31, v192
	s_add_i32 s10, s10, s76
	v_lshlrev_b64 v[128:129], 11, v[192:193]
	v_lshl_or_b32 v168, s10, 8, v170
	v_lshl_add_u64 v[128:129], s[22:23], 0, v[128:129]
	v_lshl_add_u64 v[136:137], v[168:169], 2, v[128:129]
	v_mov_b32_e32 v206, v136
	v_mov_b32_e32 v207, v137
	global_load_dwordx4 v[132:135], v[136:137], off offset:16
	global_load_dwordx4 v[144:147], v[136:137], off
	global_load_dwordx4 v[128:131], v[136:137], off offset:528
	s_nop 0
	global_load_dwordx4 v[136:139], v[136:137], off offset:512
	s_mov_b32 s100, 0x8000
	s_mov_b32 s101, 0
	v_lshl_add_u64 v[204:205], v[206:207], 0, s[100:101]
	global_load_dwordx4 v[196:199], v[204:205], off offset:16
	global_load_dwordx4 v[200:203], v[204:205], off
	s_mov_b32 s100, 0x8000
	s_mov_b32 s101, 0
	v_lshl_add_u64 v[204:205], v[206:207], 0, s[100:101]
	global_load_dwordx4 v[214:217], v[204:205], off offset:528
	global_load_dwordx4 v[218:221], v[204:205], off offset:512
	s_mov_b32 s100, 0x10000
	s_mov_b32 s101, 0
	v_lshl_add_u64 v[204:205], v[206:207], 0, s[100:101]
	global_load_dwordx4 v[222:225], v[204:205], off offset:16
	global_load_dwordx4 v[226:229], v[204:205], off
	s_mov_b32 s100, 0x10000
	s_mov_b32 s101, 0
	v_lshl_add_u64 v[204:205], v[206:207], 0, s[100:101]
	global_load_dwordx4 v[230:233], v[204:205], off offset:528
	global_load_dwordx4 v[234:237], v[204:205], off offset:512
	s_mov_b64 s[8:9], -1
	s_and_b64 vcc, exec, s[42:43]
	s_cbranch_vccz .LBB0_1416
	s_waitcnt vmcnt(10)
	v_mul_f32_e32 v140, 0xbfb8aa3b, v144
	v_mul_f32_e32 v141, 0xbfb8aa3b, v145
	v_exp_f32_e32 v140, v140
	v_exp_f32_e32 v141, v141
	v_mul_f32_e32 v142, 0xbfb8aa3b, v146
	v_mul_f32_e32 v143, 0xbfb8aa3b, v147
	v_exp_f32_e32 v142, v142
	v_pk_mul_f32 v[140:141], v[124:125], v[140:141]
	v_exp_f32_e32 v143, v143
	v_cvt_pk_bf16_f32 v140, v140, v141
	v_mul_f32_e32 v141, 0xbfb8aa3b, v132
	v_exp_f32_e32 v148, v141
	v_mul_f32_e32 v141, 0xbfb8aa3b, v133
	v_exp_f32_e32 v149, v141
	v_mul_f32_e32 v141, 0xbfb8aa3b, v134
	v_exp_f32_e32 v150, v141
	v_pk_mul_f32 v[142:143], v[126:127], v[142:143]
	s_mov_b64 s[8:9], 0
	v_cvt_pk_bf16_f32 v141, v142, v143
	v_pk_mul_f32 v[142:143], v[120:121], v[148:149]
	v_mul_f32_e32 v148, v122, v150
	v_cvt_pk_bf16_f32 v142, v142, v143
	v_mov_b32_e32 v149, v123
.LBB0_1416:
	s_andn2_b64 vcc, exec, s[8:9]
	s_mov_b32 s8, 0xbfb8aa3b
	s_cbranch_vccnz .LBB0_1418
	s_waitcnt vmcnt(10)
	v_mul_f32_e32 v140, 0x3fb8aa3b, v144
	v_mul_f32_e32 v141, 0x3fb8aa3b, v145
	v_exp_f32_e32 v140, v140
	v_exp_f32_e32 v141, v141
	v_pk_mul_f32 v[142:143], v[124:125], s[34:35] op_sel_hi:[1,0]
	v_mul_f32_e32 v132, 0x3fb8aa3b, v132
	v_mul_f32_e32 v133, 0x3fb8aa3b, v133
	v_pk_mul_f32 v[140:141], v[142:143], v[140:141]
	v_exp_f32_e32 v132, v132
	v_cvt_pk_bf16_f32 v140, v140, v141
	v_mul_f32_e32 v141, 0x3fb8aa3b, v146
	v_exp_f32_e32 v142, v141
	v_mul_f32_e32 v141, 0x3fb8aa3b, v147
	v_exp_f32_e32 v143, v141
	v_exp_f32_e32 v133, v133
	v_pk_mul_f32 v[144:145], v[126:127], s[34:35] op_sel_hi:[1,0]
	v_mul_f32_e32 v134, 0x3fb8aa3b, v134
	v_pk_mul_f32 v[142:143], v[144:145], v[142:143]
	v_exp_f32_e32 v190, v134
	v_cvt_pk_bf16_f32 v141, v142, v143
	v_pk_mul_f32 v[142:143], v[120:121], s[34:35] op_sel_hi:[1,0]
	s_mov_b32 s8, 0x3fb8aa3b
	v_pk_mul_f32 v[132:133], v[142:143], v[132:133]
	s_nop 0
	v_cvt_pk_bf16_f32 v142, v132, v133
	v_mul_f32_e32 v132, 0x3db504f3, v122
	v_mov_b32_e32 v133, v123
	v_pk_mul_f32 v[148:149], v[132:133], v[190:191]
.LBB0_1418:
	s_and_b64 s[2:3], s[2:3], exec
	s_cselect_b32 s2, s72, 0x47188000
	v_readlane_b32 s80, v252, 28
	v_readlane_b32 s81, v252, 29
	s_add_u32 s2, s80, s2
	s_addc_u32 s3, s81, 0
	s_ashr_i32 s9, s15, 9
	s_and_b32 s33, s9, -4
	s_lshl_b32 s17, s10, 1
	s_waitcnt vmcnt(10)
	v_mul_f32_e32 v132, s8, v135
	s_add_i32 s10, s33, s17
	v_exp_f32_e32 v132, v132
	s_ashr_i32 s11, s10, 31
	v_lshlrev_b32_e32 v133, 7, v192
	s_lshl_b64 s[8:9], s[10:11], 19
	v_and_b32_e32 v156, 0x3e780, v133
	s_add_u32 s10, s2, s8
	v_mul_f32_e32 v132, v149, v132
	s_addc_u32 s11, s3, s9
	v_lshlrev_b32_e32 v150, 1, v156
	v_mov_b32_e32 v151, v169
	v_cvt_pk_bf16_f32 v143, v148, v132
	v_lshl_add_u64 v[132:133], s[10:11], 0, v[150:151]
	v_lshlrev_b32_e32 v148, 1, v170
	v_mov_b32_e32 v149, v169
	v_lshl_add_u64 v[132:133], v[132:133], 0, v[148:149]
	global_store_dwordx4 v[132:133], v[140:143], off nt
	v_or_b32_e32 v132, 16, v192
	v_ashrrev_i32_e32 v133, 31, v132
	v_lshlrev_b64 v[132:133], 11, v[132:133]
	v_lshl_add_u64 v[132:133], s[22:23], 0, v[132:133]
	v_lshl_add_u64 v[152:153], v[168:169], 2, v[132:133]
	s_waitcnt vmcnt(7)
	v_mov_b32_e32 v132, v196
	v_mov_b32_e32 v133, v197
	v_mov_b32_e32 v134, v198
	v_mov_b32_e32 v135, v199
	v_mov_b32_e32 v140, v200
	v_mov_b32_e32 v141, v201
	v_mov_b32_e32 v142, v202
	v_mov_b32_e32 v143, v203
	s_mov_b32 s100, 0x18000
	s_mov_b32 s101, 0
	v_lshl_add_u64 v[204:205], v[206:207], 0, s[100:101]
	global_load_dwordx4 v[196:199], v[204:205], off offset:16
	global_load_dwordx4 v[200:203], v[204:205], off
	v_cndmask_b32_e64 v144, 0, 1, s[42:43]
	v_cmp_ne_u32_e64 s[8:9], 1, v144
	s_andn2_b64 vcc, exec, s[42:43]
	s_mov_b64 s[42:43], -1
	v_readlane_b32 s82, v252, 30
	v_readlane_b32 s83, v252, 31
	s_cbranch_vccnz .LBB0_1420
	v_mul_f32_e32 v144, 0xbfb8aa3b, v136
	v_mul_f32_e32 v145, 0xbfb8aa3b, v137
	v_exp_f32_e32 v144, v144
	v_exp_f32_e32 v145, v145
	v_mul_f32_e32 v146, 0xbfb8aa3b, v138
	v_mul_f32_e32 v147, 0xbfb8aa3b, v139
	v_exp_f32_e32 v146, v146
	v_pk_mul_f32 v[144:145], v[116:117], v[144:145]
	v_exp_f32_e32 v147, v147
	v_cvt_pk_bf16_f32 v144, v144, v145
	v_mul_f32_e32 v145, 0xbfb8aa3b, v128
	v_exp_f32_e32 v154, v145
	v_mul_f32_e32 v145, 0xbfb8aa3b, v129
	v_exp_f32_e32 v155, v145
	v_mul_f32_e32 v145, 0xbfb8aa3b, v130
	v_exp_f32_e32 v149, v145
	v_pk_mul_f32 v[146:147], v[118:119], v[146:147]
	s_mov_b64 s[42:43], 0
	v_cvt_pk_bf16_f32 v145, v146, v147
	v_pk_mul_f32 v[146:147], v[112:113], v[154:155]
	v_mul_f32_e32 v154, v114, v149
	v_cvt_pk_bf16_f32 v146, v146, v147
	v_mov_b32_e32 v155, v115

;     __device__ __forceinline__ void operator()(const f32x4 (&acc)[2][2][4][2], const Unit& u, int wr, int wc, int fr, int fq) const {
;     ...
;         } else if (u.pn < 16) {
;             const bool isq = u.pn < 14;
;             const int cb = (u.pn - (isq ? 12 : 14)) * 256;
;             bf16_t* d0 = (bf16_t*)(ws + (isq ? WS_QG : WS_KG));
;             f32x4 bc[2][2];
;     ...
;             BC_LOAD(0, 0);
; #pragma unroll
;             for (int g = 0; g < 16; ++g) {
;                 const int ai = g >> 3, m = (g >> 1) & 3, bj = g & 1;
;                 const int r = row0 + ai * HALF + m * 16;
;                 if (g + 1 < 16) BC_LOAD((g + 1) & 1, g + 1);
;                 {
;                     {
;                         const int col = cb + bj * HALF + lc;
;                         const size_t hoff = ((size_t)((r >> 11) * 4 + (col >> 7)) * SEQ + (r & (SEQ - 1))) * 128 + (col & 127);
;                         const f32x4 b0 = bc[g & 1][0], b1 = bc[g & 1][1];
;                         const f32x4 v0 = acc[ai][bj][m][0], v1 = acc[ai][bj][m][1];
;                         const float L2E = 1.4426950408889634f;
;                         if (isq) {
;                             const float s = 0.08838834764831845f;
;                             u32x4 o; o[0] = cvt_pk_bf16(v0[0] * s * __builtin_amdgcn_exp2f(b0[0] * L2E), v0[1] * s * __builtin_amdgcn_exp2f(b0[1] * L2E));
;                             o[1] = cvt_pk_bf16(v0[2] * s * __builtin_amdgcn_exp2f(b0[2] * L2E), v0[3] * s * __builtin_amdgcn_exp2f(b0[3] * L2E));
;                             o[2] = cvt_pk_bf16(v1[0] * s * __builtin_amdgcn_exp2f(b1[0] * L2E), v1[1] * s * __builtin_amdgcn_exp2f(b1[1] * L2E));
;                             o[3] = cvt_pk_bf16(v1[2] * s * __builtin_amdgcn_exp2f(b1[2] * L2E), v1[3] * s * __builtin_amdgcn_exp2f(b1[3] * L2E));
;                             __builtin_nontemporal_store(o, (u32x4*)(d0 + hoff));
;                         } else {
;                             u32x4 o;
;                             o[0] = cvt_pk_bf16(v0[0] * __builtin_amdgcn_exp2f(-b0[0] * L2E), v0[1] * __builtin_amdgcn_exp2f(-b0[1] * L2E));
;                             o[1] = cvt_pk_bf16(v0[2] * __builtin_amdgcn_exp2f(-b0[2] * L2E), v0[3] * __builtin_amdgcn_exp2f(-b0[3] * L2E));
.LBB0_1422:
	v_mul_f32_e32 v128, s18, v131
	s_or_b32 s18, s17, 1
	v_exp_f32_e32 v128, v128
	s_add_i32 s42, s33, s18
	s_ashr_i32 s43, s42, 31
	s_lshl_b64 s[42:43], s[42:43], 19
	s_add_u32 s42, s2, s42
	v_mul_f32_e32 v128, v155, v128
	s_addc_u32 s43, s3, s43
	v_mov_b32_e32 v151, v169
	v_cvt_pk_bf16_f32 v147, v154, v128
	v_lshl_add_u64 v[128:129], s[42:43], 0, v[150:151]
	v_mov_b32_e32 v149, v169
	v_lshl_add_u64 v[128:129], v[128:129], 0, v[148:149]
	global_store_dwordx4 v[128:129], v[144:147], off nt
	s_waitcnt vmcnt(8)
	v_mov_b32_e32 v128, v214
	v_mov_b32_e32 v129, v215
	v_mov_b32_e32 v130, v216
	v_mov_b32_e32 v131, v217
	v_mov_b32_e32 v136, v218
	v_mov_b32_e32 v137, v219
	v_mov_b32_e32 v138, v220
	v_mov_b32_e32 v139, v221
	s_mov_b32 s100, 0x18000
	s_mov_b32 s101, 0
	v_lshl_add_u64 v[204:205], v[206:207], 0, s[100:101]
	global_load_dwordx4 v[214:217], v[204:205], off offset:528
	global_load_dwordx4 v[218:221], v[204:205], off offset:512
	s_nop 0
	s_and_b64 vcc, exec, s[8:9]
	s_mov_b64 s[48:49], -1
	s_cbranch_vccnz .LBB0_1424
	v_mul_f32_e32 v144, 0xbfb8aa3b, v140
	v_mul_f32_e32 v145, 0xbfb8aa3b, v141
	v_exp_f32_e32 v144, v144
	v_exp_f32_e32 v145, v145
	v_mul_f32_e32 v146, 0xbfb8aa3b, v142
	v_mul_f32_e32 v147, 0xbfb8aa3b, v143
	v_exp_f32_e32 v146, v146
	v_pk_mul_f32 v[144:145], v[108:109], v[144:145]
	v_exp_f32_e32 v147, v147
	v_cvt_pk_bf16_f32 v144, v144, v145
	v_mul_f32_e32 v145, 0xbfb8aa3b, v132
	v_exp_f32_e32 v150, v145
	v_mul_f32_e32 v145, 0xbfb8aa3b, v133
	v_exp_f32_e32 v151, v145
	v_mul_f32_e32 v145, 0xbfb8aa3b, v134
	v_exp_f32_e32 v149, v145
	v_pk_mul_f32 v[146:147], v[110:111], v[146:147]
	s_mov_b64 s[48:49], 0
	v_cvt_pk_bf16_f32 v145, v146, v147
	v_pk_mul_f32 v[146:147], v[104:105], v[150:151]
	v_mul_f32_e32 v152, v106, v149
	v_cvt_pk_bf16_f32 v146, v146, v147
	v_mov_b32_e32 v153, v107
.LBB0_1424:
	s_andn2_b64 vcc, exec, s[48:49]
	s_mov_b32 s33, 0xbfb8aa3b
	s_cbranch_vccnz .LBB0_1426
	v_mul_f32_e32 v140, 0x3fb8aa3b, v140
	v_mul_f32_e32 v141, 0x3fb8aa3b, v141
	v_exp_f32_e32 v140, v140
	v_exp_f32_e32 v141, v141
	v_pk_mul_f32 v[144:145], v[108:109], s[34:35] op_sel_hi:[1,0]
	v_mul_f32_e32 v132, 0x3fb8aa3b, v132
	v_mul_f32_e32 v133, 0x3fb8aa3b, v133
	v_pk_mul_f32 v[140:141], v[144:145], v[140:141]
	v_exp_f32_e32 v132, v132
	v_cvt_pk_bf16_f32 v144, v140, v141
	v_mul_f32_e32 v140, 0x3fb8aa3b, v142
	v_mul_f32_e32 v141, 0x3fb8aa3b, v143
	v_exp_f32_e32 v140, v140
	v_exp_f32_e32 v141, v141
	v_exp_f32_e32 v133, v133
	v_pk_mul_f32 v[142:143], v[110:111], s[34:35] op_sel_hi:[1,0]
	v_mul_f32_e32 v134, 0x3fb8aa3b, v134
	v_pk_mul_f32 v[140:141], v[142:143], v[140:141]
	v_exp_f32_e32 v190, v134
	v_cvt_pk_bf16_f32 v145, v140, v141
	v_pk_mul_f32 v[140:141], v[104:105], s[34:35] op_sel_hi:[1,0]
	s_mov_b32 s33, 0x3fb8aa3b
	v_pk_mul_f32 v[132:133], v[140:141], v[132:133]
	s_nop 0
	v_cvt_pk_bf16_f32 v146, v132, v133
	v_mul_f32_e32 v132, 0x3db504f3, v106
	v_mov_b32_e32 v133, v107
	v_pk_mul_f32 v[152:153], v[132:133], v[190:191]
.LBB0_1426:
	v_mul_f32_e32 v132, s33, v135
	v_exp_f32_e32 v132, v132
	v_or_b32_e32 v133, 0x800, v156
	v_mov_b32_e32 v151, v169
	v_lshlrev_b32_e32 v150, 1, v133
	v_mul_f32_e32 v132, v153, v132
	v_cvt_pk_bf16_f32 v147, v152, v132
	v_lshl_add_u64 v[132:133], s[10:11], 0, v[150:151]
	v_mov_b32_e32 v149, v169
	v_lshl_add_u64 v[132:133], v[132:133], 0, v[148:149]
	global_store_dwordx4 v[132:133], v[144:147], off nt
	v_or_b32_e32 v132, 32, v192
	v_ashrrev_i32_e32 v133, 31, v132
	v_lshlrev_b64 v[132:133], 11, v[132:133]
	v_lshl_add_u64 v[132:133], s[22:23], 0, v[132:133]
	v_lshl_add_u64 v[152:153], v[168:169], 2, v[132:133]
	s_waitcnt vmcnt(9)
	v_mov_b32_e32 v132, v222
	v_mov_b32_e32 v133, v223
	v_mov_b32_e32 v134, v224
	v_mov_b32_e32 v135, v225
	v_mov_b32_e32 v140, v226
	v_mov_b32_e32 v141, v227
	v_mov_b32_e32 v142, v228
	v_mov_b32_e32 v143, v229
	s_mov_b32 s100, 0x40000
	s_mov_b32 s101, 0
	v_lshl_add_u64 v[204:205], v[206:207], 0, s[100:101]
	global_load_dwordx4 v[222:225], v[204:205], off offset:16
	global_load_dwordx4 v[226:229], v[204:205], off
	s_and_b64 vcc, exec, s[8:9]
	s_mov_b64 s[48:49], -1
	s_cbranch_vccnz .LBB0_1428
	v_mul_f32_e32 v144, 0xbfb8aa3b, v136
	v_mul_f32_e32 v145, 0xbfb8aa3b, v137
	v_exp_f32_e32 v144, v144
	v_exp_f32_e32 v145, v145
	v_mul_f32_e32 v146, 0xbfb8aa3b, v138
	v_mul_f32_e32 v147, 0xbfb8aa3b, v139
	v_exp_f32_e32 v146, v146
	v_pk_mul_f32 v[144:145], v[100:101], v[144:145]
	v_exp_f32_e32 v147, v147
	v_cvt_pk_bf16_f32 v144, v144, v145
	v_mul_f32_e32 v145, 0xbfb8aa3b, v128
	v_exp_f32_e32 v154, v145
	v_mul_f32_e32 v145, 0xbfb8aa3b, v129
	v_exp_f32_e32 v155, v145
	v_mul_f32_e32 v145, 0xbfb8aa3b, v130
	v_exp_f32_e32 v149, v145
	v_pk_mul_f32 v[146:147], v[102:103], v[146:147]
	s_mov_b64 s[48:49], 0
	v_cvt_pk_bf16_f32 v145, v146, v147
	v_pk_mul_f32 v[146:147], v[96:97], v[154:155]
	v_mul_f32_e32 v154, v98, v149
	v_cvt_pk_bf16_f32 v146, v146, v147
	v_mov_b32_e32 v155, v99

;     __device__ __forceinline__ void operator()(const f32x4 (&acc)[2][2][4][2], const Unit& u, int wr, int wc, int fr, int fq) const {
;     ...
;         } else if (u.pn < 16) {
;             const bool isq = u.pn < 14;
;             const int cb = (u.pn - (isq ? 12 : 14)) * 256;
;             bf16_t* d0 = (bf16_t*)(ws + (isq ? WS_QG : WS_KG));
;             f32x4 bc[2][2];
;     ...
;             BC_LOAD(0, 0);
; #pragma unroll
;             for (int g = 0; g < 16; ++g) {
;                 const int ai = g >> 3, m = (g >> 1) & 3, bj = g & 1;
;                 const int r = row0 + ai * HALF + m * 16;
;                 if (g + 1 < 16) BC_LOAD((g + 1) & 1, g + 1);
;                 {
;                     {
;                         const int col = cb + bj * HALF + lc;
;                         const size_t hoff = ((size_t)((r >> 11) * 4 + (col >> 7)) * SEQ + (r & (SEQ - 1))) * 128 + (col & 127);
;                         const f32x4 b0 = bc[g & 1][0], b1 = bc[g & 1][1];
;                         const f32x4 v0 = acc[ai][bj][m][0], v1 = acc[ai][bj][m][1];
;                         const float L2E = 1.4426950408889634f;
;                         if (isq) {
;                             const float s = 0.08838834764831845f;
;                             u32x4 o; o[0] = cvt_pk_bf16(v0[0] * s * __builtin_amdgcn_exp2f(b0[0] * L2E), v0[1] * s * __builtin_amdgcn_exp2f(b0[1] * L2E));
;                             o[1] = cvt_pk_bf16(v0[2] * s * __builtin_amdgcn_exp2f(b0[2] * L2E), v0[3] * s * __builtin_amdgcn_exp2f(b0[3] * L2E));
;                             o[2] = cvt_pk_bf16(v1[0] * s * __builtin_amdgcn_exp2f(b1[0] * L2E), v1[1] * s * __builtin_amdgcn_exp2f(b1[1] * L2E));
;                             o[3] = cvt_pk_bf16(v1[2] * s * __builtin_amdgcn_exp2f(b1[2] * L2E), v1[3] * s * __builtin_amdgcn_exp2f(b1[3] * L2E));
;                             __builtin_nontemporal_store(o, (u32x4*)(d0 + hoff));
;                         } else {
;                             u32x4 o;
;                             o[0] = cvt_pk_bf16(v0[0] * __builtin_amdgcn_exp2f(-b0[0] * L2E), v0[1] * __builtin_amdgcn_exp2f(-b0[1] * L2E));
;                             o[1] = cvt_pk_bf16(v0[2] * __builtin_amdgcn_exp2f(-b0[2] * L2E), v0[3] * __builtin_amdgcn_exp2f(-b0[3] * L2E));
.LBB0_1430:
	v_mul_f32_e32 v128, s33, v131
	v_exp_f32_e32 v130, v128
	v_mov_b32_e32 v151, v169
	v_mov_b32_e32 v149, v169
	v_lshl_add_u64 v[128:129], s[42:43], 0, v[150:151]
	v_mul_f32_e32 v130, v155, v130
	v_cvt_pk_bf16_f32 v147, v154, v130
	v_lshl_add_u64 v[128:129], v[128:129], 0, v[148:149]
	global_store_dwordx4 v[128:129], v[144:147], off nt
	s_waitcnt vmcnt(10)
	v_mov_b32_e32 v128, v230
	v_mov_b32_e32 v129, v231
	v_mov_b32_e32 v130, v232
	v_mov_b32_e32 v131, v233
	v_mov_b32_e32 v136, v234
	v_mov_b32_e32 v137, v235
	v_mov_b32_e32 v138, v236
	v_mov_b32_e32 v139, v237
	s_mov_b32 s100, 0x40000
	s_mov_b32 s101, 0
	v_lshl_add_u64 v[204:205], v[206:207], 0, s[100:101]
	global_load_dwordx4 v[230:233], v[204:205], off offset:528
	global_load_dwordx4 v[234:237], v[204:205], off offset:512
	s_nop 0
	s_and_b64 vcc, exec, s[8:9]
	s_mov_b64 s[48:49], -1
	s_cbranch_vccnz .LBB0_1432
	v_mul_f32_e32 v144, 0xbfb8aa3b, v140
	v_mul_f32_e32 v145, 0xbfb8aa3b, v141
	v_exp_f32_e32 v144, v144
	v_exp_f32_e32 v145, v145
	v_mul_f32_e32 v146, 0xbfb8aa3b, v142
	v_mul_f32_e32 v147, 0xbfb8aa3b, v143
	v_exp_f32_e32 v146, v146
	v_pk_mul_f32 v[144:145], v[92:93], v[144:145]
	v_exp_f32_e32 v147, v147
	v_cvt_pk_bf16_f32 v144, v144, v145
	v_mul_f32_e32 v145, 0xbfb8aa3b, v132
	v_exp_f32_e32 v150, v145
	v_mul_f32_e32 v145, 0xbfb8aa3b, v133
	v_exp_f32_e32 v151, v145
	v_mul_f32_e32 v145, 0xbfb8aa3b, v134
	v_exp_f32_e32 v149, v145
	v_pk_mul_f32 v[146:147], v[94:95], v[146:147]
	s_mov_b64 s[48:49], 0
	v_cvt_pk_bf16_f32 v145, v146, v147
	v_pk_mul_f32 v[146:147], v[88:89], v[150:151]
	v_mul_f32_e32 v152, v90, v149
	v_cvt_pk_bf16_f32 v146, v146, v147
	v_mov_b32_e32 v153, v91
.LBB0_1432:
	s_andn2_b64 vcc, exec, s[48:49]
	s_mov_b32 s33, 0xbfb8aa3b
	s_cbranch_vccnz .LBB0_1434
	v_mul_f32_e32 v140, 0x3fb8aa3b, v140
	v_mul_f32_e32 v141, 0x3fb8aa3b, v141
	v_exp_f32_e32 v140, v140
	v_exp_f32_e32 v141, v141
	v_pk_mul_f32 v[144:145], v[92:93], s[34:35] op_sel_hi:[1,0]
	v_mul_f32_e32 v132, 0x3fb8aa3b, v132
	v_mul_f32_e32 v133, 0x3fb8aa3b, v133
	v_pk_mul_f32 v[140:141], v[144:145], v[140:141]
	v_exp_f32_e32 v132, v132
	v_cvt_pk_bf16_f32 v144, v140, v141
	v_mul_f32_e32 v140, 0x3fb8aa3b, v142
	v_mul_f32_e32 v141, 0x3fb8aa3b, v143
	v_exp_f32_e32 v140, v140
	v_exp_f32_e32 v141, v141
	v_exp_f32_e32 v133, v133
	v_pk_mul_f32 v[142:143], v[94:95], s[34:35] op_sel_hi:[1,0]
	v_mul_f32_e32 v134, 0x3fb8aa3b, v134
	v_pk_mul_f32 v[140:141], v[142:143], v[140:141]
	v_exp_f32_e32 v190, v134
	v_cvt_pk_bf16_f32 v145, v140, v141
	v_pk_mul_f32 v[140:141], v[88:89], s[34:35] op_sel_hi:[1,0]
	s_mov_b32 s33, 0x3fb8aa3b
	v_pk_mul_f32 v[132:133], v[140:141], v[132:133]
	s_nop 0
	v_cvt_pk_bf16_f32 v146, v132, v133
	v_mul_f32_e32 v132, 0x3db504f3, v90
	v_mov_b32_e32 v133, v91
	v_pk_mul_f32 v[152:153], v[132:133], v[190:191]
.LBB0_1434:
	v_mul_f32_e32 v132, s33, v135
	v_exp_f32_e32 v132, v132
	v_or_b32_e32 v133, 0x1000, v156
	v_mov_b32_e32 v151, v169
	v_lshlrev_b32_e32 v150, 1, v133
	v_mul_f32_e32 v132, v153, v132
	v_cvt_pk_bf16_f32 v147, v152, v132
	v_lshl_add_u64 v[132:133], s[10:11], 0, v[150:151]
	v_mov_b32_e32 v149, v169
	v_lshl_add_u64 v[132:133], v[132:133], 0, v[148:149]
	global_store_dwordx4 v[132:133], v[144:147], off nt
	v_or_b32_e32 v132, 48, v192
	v_ashrrev_i32_e32 v133, 31, v132
	v_lshlrev_b64 v[132:133], 11, v[132:133]
	v_lshl_add_u64 v[132:133], s[22:23], 0, v[132:133]
	v_lshl_add_u64 v[152:153], v[168:169], 2, v[132:133]
	s_waitcnt vmcnt(10)
	v_mov_b32_e32 v132, v196
	v_mov_b32_e32 v133, v197
	v_mov_b32_e32 v134, v198
	v_mov_b32_e32 v135, v199
	v_mov_b32_e32 v140, v200
	v_mov_b32_e32 v141, v201
	v_mov_b32_e32 v142, v202
	v_mov_b32_e32 v143, v203
	s_mov_b32 s100, 0x48000
	s_mov_b32 s101, 0
	v_lshl_add_u64 v[204:205], v[206:207], 0, s[100:101]
	global_load_dwordx4 v[196:199], v[204:205], off offset:16
	global_load_dwordx4 v[200:203], v[204:205], off
	s_and_b64 vcc, exec, s[8:9]
	s_mov_b64 s[48:49], -1
	s_cbranch_vccnz .LBB0_1436
	v_mul_f32_e32 v144, 0xbfb8aa3b, v136
	v_mul_f32_e32 v145, 0xbfb8aa3b, v137
	v_exp_f32_e32 v144, v144
	v_exp_f32_e32 v145, v145
	v_mul_f32_e32 v146, 0xbfb8aa3b, v138
	v_mul_f32_e32 v147, 0xbfb8aa3b, v139
	v_exp_f32_e32 v146, v146
	v_pk_mul_f32 v[144:145], v[84:85], v[144:145]
	v_exp_f32_e32 v147, v147
	v_cvt_pk_bf16_f32 v144, v144, v145
	v_mul_f32_e32 v145, 0xbfb8aa3b, v128
	v_exp_f32_e32 v154, v145
	v_mul_f32_e32 v145, 0xbfb8aa3b, v129
	v_exp_f32_e32 v155, v145
	v_mul_f32_e32 v145, 0xbfb8aa3b, v130
	v_exp_f32_e32 v149, v145
	v_pk_mul_f32 v[146:147], v[86:87], v[146:147]
	s_mov_b64 s[48:49], 0
	v_cvt_pk_bf16_f32 v145, v146, v147
	v_pk_mul_f32 v[146:147], v[80:81], v[154:155]
	v_mul_f32_e32 v154, v82, v149
	v_cvt_pk_bf16_f32 v146, v146, v147
	v_mov_b32_e32 v155, v83

;     __device__ __forceinline__ void operator()(const f32x4 (&acc)[2][2][4][2], const Unit& u, int wr, int wc, int fr, int fq) const {
;     ...
;         } else if (u.pn < 16) {
;             const bool isq = u.pn < 14;
;             const int cb = (u.pn - (isq ? 12 : 14)) * 256;
;             bf16_t* d0 = (bf16_t*)(ws + (isq ? WS_QG : WS_KG));
;             f32x4 bc[2][2];
;     ...
;             BC_LOAD(0, 0);
; #pragma unroll
;             for (int g = 0; g < 16; ++g) {
;                 const int ai = g >> 3, m = (g >> 1) & 3, bj = g & 1;
;                 const int r = row0 + ai * HALF + m * 16;
;                 if (g + 1 < 16) BC_LOAD((g + 1) & 1, g + 1);
;                 {
;                     {
;                         const int col = cb + bj * HALF + lc;
;                         const size_t hoff = ((size_t)((r >> 11) * 4 + (col >> 7)) * SEQ + (r & (SEQ - 1))) * 128 + (col & 127);
;                         const f32x4 b0 = bc[g & 1][0], b1 = bc[g & 1][1];
;                         const f32x4 v0 = acc[ai][bj][m][0], v1 = acc[ai][bj][m][1];
;                         const float L2E = 1.4426950408889634f;
;                         if (isq) {
;                             const float s = 0.08838834764831845f;
;                             u32x4 o; o[0] = cvt_pk_bf16(v0[0] * s * __builtin_amdgcn_exp2f(b0[0] * L2E), v0[1] * s * __builtin_amdgcn_exp2f(b0[1] * L2E));
;                             o[1] = cvt_pk_bf16(v0[2] * s * __builtin_amdgcn_exp2f(b0[2] * L2E), v0[3] * s * __builtin_amdgcn_exp2f(b0[3] * L2E));
;                             o[2] = cvt_pk_bf16(v1[0] * s * __builtin_amdgcn_exp2f(b1[0] * L2E), v1[1] * s * __builtin_amdgcn_exp2f(b1[1] * L2E));
;                             o[3] = cvt_pk_bf16(v1[2] * s * __builtin_amdgcn_exp2f(b1[2] * L2E), v1[3] * s * __builtin_amdgcn_exp2f(b1[3] * L2E));
;                             __builtin_nontemporal_store(o, (u32x4*)(d0 + hoff));
;                         } else {
;                             u32x4 o;
;                             o[0] = cvt_pk_bf16(v0[0] * __builtin_amdgcn_exp2f(-b0[0] * L2E), v0[1] * __builtin_amdgcn_exp2f(-b0[1] * L2E));
;                             o[1] = cvt_pk_bf16(v0[2] * __builtin_amdgcn_exp2f(-b0[2] * L2E), v0[3] * __builtin_amdgcn_exp2f(-b0[3] * L2E));
.LBB0_1438:
	v_mul_f32_e32 v128, s33, v131
	v_exp_f32_e32 v130, v128
	v_mov_b32_e32 v151, v169
	v_mov_b32_e32 v149, v169
	v_lshl_add_u64 v[128:129], s[42:43], 0, v[150:151]
	v_mul_f32_e32 v130, v155, v130
	v_cvt_pk_bf16_f32 v147, v154, v130
	v_lshl_add_u64 v[128:129], v[128:129], 0, v[148:149]
	global_store_dwordx4 v[128:129], v[144:147], off nt
	s_waitcnt vmcnt(10)
	v_mov_b32_e32 v128, v214
	v_mov_b32_e32 v129, v215
	v_mov_b32_e32 v130, v216
	v_mov_b32_e32 v131, v217
	v_mov_b32_e32 v136, v218
	v_mov_b32_e32 v137, v219
	v_mov_b32_e32 v138, v220
	v_mov_b32_e32 v139, v221
	s_mov_b32 s100, 0x48000
	s_mov_b32 s101, 0
	v_lshl_add_u64 v[204:205], v[206:207], 0, s[100:101]
	global_load_dwordx4 v[214:217], v[204:205], off offset:528
	global_load_dwordx4 v[218:221], v[204:205], off offset:512
	s_nop 0
	s_and_b64 vcc, exec, s[8:9]
	s_mov_b64 s[48:49], -1
	s_cbranch_vccnz .LBB0_1440
	v_mul_f32_e32 v144, 0xbfb8aa3b, v140
	v_mul_f32_e32 v145, 0xbfb8aa3b, v141
	v_exp_f32_e32 v144, v144
	v_exp_f32_e32 v145, v145
	v_mul_f32_e32 v146, 0xbfb8aa3b, v142
	v_mul_f32_e32 v147, 0xbfb8aa3b, v143
	v_exp_f32_e32 v146, v146
	v_pk_mul_f32 v[144:145], v[76:77], v[144:145]
	v_exp_f32_e32 v147, v147
	v_cvt_pk_bf16_f32 v144, v144, v145
	v_mul_f32_e32 v145, 0xbfb8aa3b, v132
	v_exp_f32_e32 v150, v145
	v_mul_f32_e32 v145, 0xbfb8aa3b, v133
	v_exp_f32_e32 v151, v145
	v_mul_f32_e32 v145, 0xbfb8aa3b, v134
	v_exp_f32_e32 v149, v145
	v_pk_mul_f32 v[146:147], v[78:79], v[146:147]
	s_mov_b64 s[48:49], 0
	v_cvt_pk_bf16_f32 v145, v146, v147
	v_pk_mul_f32 v[146:147], v[72:73], v[150:151]
	v_mul_f32_e32 v150, v74, v149
	v_cvt_pk_bf16_f32 v146, v146, v147
	v_mov_b32_e32 v151, v75
.LBB0_1440:
	s_andn2_b64 vcc, exec, s[48:49]
	s_mov_b32 s33, 0xbfb8aa3b
	s_cbranch_vccnz .LBB0_1442
	v_mul_f32_e32 v140, 0x3fb8aa3b, v140
	v_mul_f32_e32 v141, 0x3fb8aa3b, v141
	v_exp_f32_e32 v140, v140
	v_exp_f32_e32 v141, v141
	v_pk_mul_f32 v[144:145], v[76:77], s[34:35] op_sel_hi:[1,0]
	v_mul_f32_e32 v132, 0x3fb8aa3b, v132
	v_mul_f32_e32 v133, 0x3fb8aa3b, v133
	v_pk_mul_f32 v[140:141], v[144:145], v[140:141]
	v_exp_f32_e32 v132, v132
	v_cvt_pk_bf16_f32 v144, v140, v141
	v_mul_f32_e32 v140, 0x3fb8aa3b, v142
	v_mul_f32_e32 v141, 0x3fb8aa3b, v143
	v_exp_f32_e32 v140, v140
	v_exp_f32_e32 v141, v141
	v_exp_f32_e32 v133, v133
	v_pk_mul_f32 v[142:143], v[78:79], s[34:35] op_sel_hi:[1,0]
	v_mul_f32_e32 v134, 0x3fb8aa3b, v134
	v_pk_mul_f32 v[140:141], v[142:143], v[140:141]
	v_exp_f32_e32 v190, v134
	v_cvt_pk_bf16_f32 v145, v140, v141
	v_pk_mul_f32 v[140:141], v[72:73], s[34:35] op_sel_hi:[1,0]
	s_mov_b32 s33, 0x3fb8aa3b
	v_pk_mul_f32 v[132:133], v[140:141], v[132:133]
	s_nop 0
	v_cvt_pk_bf16_f32 v146, v132, v133
	v_mul_f32_e32 v132, 0x3db504f3, v74
	v_mov_b32_e32 v133, v75
	v_pk_mul_f32 v[150:151], v[132:133], v[190:191]
.LBB0_1442:
	v_mul_f32_e32 v132, s33, v135
	v_exp_f32_e32 v132, v132
	v_or_b32_e32 v133, 0x1800, v156
	v_mov_b32_e32 v153, v169
	v_lshlrev_b32_e32 v152, 1, v133
	v_mul_f32_e32 v132, v151, v132
	v_cvt_pk_bf16_f32 v147, v150, v132
	v_lshl_add_u64 v[132:133], s[10:11], 0, v[152:153]
	v_mov_b32_e32 v149, v169
	v_add_u32_e32 v150, 0x80, v192
	v_lshl_add_u64 v[132:133], v[132:133], 0, v[148:149]
	v_ashrrev_i32_e32 v151, 31, v150
	global_store_dwordx4 v[132:133], v[144:147], off nt
	v_lshlrev_b64 v[132:133], 11, v[150:151]
	v_lshl_add_u64 v[132:133], s[22:23], 0, v[132:133]
	v_lshl_add_u64 v[154:155], v[168:169], 2, v[132:133]
	s_waitcnt vmcnt(10)
	v_mov_b32_e32 v132, v222
	v_mov_b32_e32 v133, v223
	v_mov_b32_e32 v134, v224
	v_mov_b32_e32 v135, v225
	v_mov_b32_e32 v140, v226
	v_mov_b32_e32 v141, v227
	v_mov_b32_e32 v142, v228
	v_mov_b32_e32 v143, v229
	s_mov_b32 s100, 0x50000
	s_mov_b32 s101, 0
	v_lshl_add_u64 v[204:205], v[206:207], 0, s[100:101]
	global_load_dwordx4 v[222:225], v[204:205], off offset:16
	global_load_dwordx4 v[226:229], v[204:205], off
	s_and_b64 vcc, exec, s[8:9]
	s_mov_b64 s[10:11], -1
	s_cbranch_vccnz .LBB0_1444
	v_mul_f32_e32 v144, 0xbfb8aa3b, v136
	v_mul_f32_e32 v145, 0xbfb8aa3b, v137
	v_exp_f32_e32 v144, v144
	v_exp_f32_e32 v145, v145
	v_mul_f32_e32 v146, 0xbfb8aa3b, v138
	v_mul_f32_e32 v147, 0xbfb8aa3b, v139
	v_exp_f32_e32 v146, v146
	v_pk_mul_f32 v[144:145], v[68:69], v[144:145]
	v_exp_f32_e32 v147, v147
	v_cvt_pk_bf16_f32 v144, v144, v145
	v_mul_f32_e32 v145, 0xbfb8aa3b, v128
	v_exp_f32_e32 v156, v145
	v_mul_f32_e32 v145, 0xbfb8aa3b, v129
	v_exp_f32_e32 v157, v145
	v_mul_f32_e32 v145, 0xbfb8aa3b, v130
	v_exp_f32_e32 v149, v145
	v_pk_mul_f32 v[146:147], v[70:71], v[146:147]
	s_mov_b64 s[10:11], 0
	v_cvt_pk_bf16_f32 v145, v146, v147
	v_pk_mul_f32 v[146:147], v[64:65], v[156:157]
	v_mul_f32_e32 v156, v66, v149
	v_cvt_pk_bf16_f32 v146, v146, v147
	v_mov_b32_e32 v157, v67

;     __device__ __forceinline__ void operator()(const f32x4 (&acc)[2][2][4][2], const Unit& u, int wr, int wc, int fr, int fq) const {
;     ...
;         } else if (u.pn < 16) {
;             const bool isq = u.pn < 14;
;             const int cb = (u.pn - (isq ? 12 : 14)) * 256;
;             bf16_t* d0 = (bf16_t*)(ws + (isq ? WS_QG : WS_KG));
;             f32x4 bc[2][2];
;     ...
;             BC_LOAD(0, 0);
; #pragma unroll
;             for (int g = 0; g < 16; ++g) {
;                 const int ai = g >> 3, m = (g >> 1) & 3, bj = g & 1;
;                 const int r = row0 + ai * HALF + m * 16;
;                 if (g + 1 < 16) BC_LOAD((g + 1) & 1, g + 1);
;                 {
;                     {
;                         const int col = cb + bj * HALF + lc;
;                         const size_t hoff = ((size_t)((r >> 11) * 4 + (col >> 7)) * SEQ + (r & (SEQ - 1))) * 128 + (col & 127);
;                         const f32x4 b0 = bc[g & 1][0], b1 = bc[g & 1][1];
;                         const f32x4 v0 = acc[ai][bj][m][0], v1 = acc[ai][bj][m][1];
;                         const float L2E = 1.4426950408889634f;
;                         if (isq) {
;                             const float s = 0.08838834764831845f;
;                             u32x4 o; o[0] = cvt_pk_bf16(v0[0] * s * __builtin_amdgcn_exp2f(b0[0] * L2E), v0[1] * s * __builtin_amdgcn_exp2f(b0[1] * L2E));
;                             o[1] = cvt_pk_bf16(v0[2] * s * __builtin_amdgcn_exp2f(b0[2] * L2E), v0[3] * s * __builtin_amdgcn_exp2f(b0[3] * L2E));
;                             o[2] = cvt_pk_bf16(v1[0] * s * __builtin_amdgcn_exp2f(b1[0] * L2E), v1[1] * s * __builtin_amdgcn_exp2f(b1[1] * L2E));
;                             o[3] = cvt_pk_bf16(v1[2] * s * __builtin_amdgcn_exp2f(b1[2] * L2E), v1[3] * s * __builtin_amdgcn_exp2f(b1[3] * L2E));
;                             __builtin_nontemporal_store(o, (u32x4*)(d0 + hoff));
;                         } else {
;                             u32x4 o;
;                             o[0] = cvt_pk_bf16(v0[0] * __builtin_amdgcn_exp2f(-b0[0] * L2E), v0[1] * __builtin_amdgcn_exp2f(-b0[1] * L2E));
;                             o[1] = cvt_pk_bf16(v0[2] * __builtin_amdgcn_exp2f(-b0[2] * L2E), v0[3] * __builtin_amdgcn_exp2f(-b0[3] * L2E));
.LBB0_1446:
	v_mul_f32_e32 v128, s10, v131
	v_exp_f32_e32 v130, v128
	v_mov_b32_e32 v153, v169
	v_mov_b32_e32 v149, v169
	v_lshl_add_u64 v[128:129], s[42:43], 0, v[152:153]
	v_mul_f32_e32 v130, v157, v130
	v_cvt_pk_bf16_f32 v147, v156, v130
	v_lshl_add_u64 v[128:129], v[128:129], 0, v[148:149]
	global_store_dwordx4 v[128:129], v[144:147], off nt
	s_waitcnt vmcnt(10)
	v_mov_b32_e32 v128, v230
	v_mov_b32_e32 v129, v231
	v_mov_b32_e32 v130, v232
	v_mov_b32_e32 v131, v233
	v_mov_b32_e32 v136, v234
	v_mov_b32_e32 v137, v235
	v_mov_b32_e32 v138, v236
	v_mov_b32_e32 v139, v237
	s_mov_b32 s100, 0x50000
	s_mov_b32 s101, 0
	v_lshl_add_u64 v[204:205], v[206:207], 0, s[100:101]
	global_load_dwordx4 v[230:233], v[204:205], off offset:528
	global_load_dwordx4 v[234:237], v[204:205], off offset:512
	s_nop 0
	s_and_b64 vcc, exec, s[8:9]
	s_mov_b64 s[10:11], -1
	s_cbranch_vccnz .LBB0_1448
	v_mul_f32_e32 v144, 0xbfb8aa3b, v140
	v_mul_f32_e32 v145, 0xbfb8aa3b, v141
	v_exp_f32_e32 v144, v144
	v_exp_f32_e32 v145, v145
	v_mul_f32_e32 v146, 0xbfb8aa3b, v142
	v_mul_f32_e32 v147, 0xbfb8aa3b, v143
	v_exp_f32_e32 v146, v146
	v_pk_mul_f32 v[144:145], v[60:61], v[144:145]
	v_exp_f32_e32 v147, v147
	v_cvt_pk_bf16_f32 v144, v144, v145
	v_mul_f32_e32 v145, 0xbfb8aa3b, v132
	v_exp_f32_e32 v152, v145
	v_mul_f32_e32 v145, 0xbfb8aa3b, v133
	v_exp_f32_e32 v153, v145
	v_mul_f32_e32 v145, 0xbfb8aa3b, v134
	v_exp_f32_e32 v149, v145
	v_pk_mul_f32 v[146:147], v[62:63], v[146:147]
	s_mov_b64 s[10:11], 0
	v_cvt_pk_bf16_f32 v145, v146, v147
	v_pk_mul_f32 v[146:147], v[56:57], v[152:153]
	v_mul_f32_e32 v152, v58, v149
	v_cvt_pk_bf16_f32 v146, v146, v147
	v_mov_b32_e32 v153, v59
.LBB0_1448:
	s_andn2_b64 vcc, exec, s[10:11]
	s_mov_b32 s10, 0xbfb8aa3b
	s_cbranch_vccnz .LBB0_1450
	v_mul_f32_e32 v140, 0x3fb8aa3b, v140
	v_mul_f32_e32 v141, 0x3fb8aa3b, v141
	v_exp_f32_e32 v140, v140
	v_exp_f32_e32 v141, v141
	v_pk_mul_f32 v[144:145], v[60:61], s[34:35] op_sel_hi:[1,0]
	v_mul_f32_e32 v132, 0x3fb8aa3b, v132
	v_mul_f32_e32 v133, 0x3fb8aa3b, v133
	v_pk_mul_f32 v[140:141], v[144:145], v[140:141]
	v_exp_f32_e32 v132, v132
	v_cvt_pk_bf16_f32 v144, v140, v141
	v_mul_f32_e32 v140, 0x3fb8aa3b, v142
	v_mul_f32_e32 v141, 0x3fb8aa3b, v143
	v_exp_f32_e32 v140, v140
	v_exp_f32_e32 v141, v141
	v_exp_f32_e32 v133, v133
	v_pk_mul_f32 v[142:143], v[62:63], s[34:35] op_sel_hi:[1,0]
	v_mul_f32_e32 v134, 0x3fb8aa3b, v134
	v_pk_mul_f32 v[140:141], v[142:143], v[140:141]
	v_exp_f32_e32 v190, v134
	v_cvt_pk_bf16_f32 v145, v140, v141
	v_pk_mul_f32 v[140:141], v[56:57], s[34:35] op_sel_hi:[1,0]
	s_mov_b32 s10, 0x3fb8aa3b
	v_pk_mul_f32 v[132:133], v[140:141], v[132:133]
	s_nop 0
	v_cvt_pk_bf16_f32 v146, v132, v133
	v_mul_f32_e32 v132, 0x3db504f3, v58
	v_mov_b32_e32 v133, v59
	v_pk_mul_f32 v[152:153], v[132:133], v[190:191]
.LBB0_1450:
	v_mul_f32_e32 v133, s10, v135
	v_ashrrev_i32_e32 v132, 9, v150
	v_exp_f32_e32 v134, v133
	v_and_b32_e32 v151, -4, v132
	v_add_u32_e32 v132, s17, v151
	v_ashrrev_i32_e32 v133, 31, v132
	v_lshlrev_b32_e32 v135, 7, v150
	v_and_b32_e32 v193, 0x3e780, v135
	v_mul_f32_e32 v134, v153, v134
	v_lshlrev_b64 v[132:133], 19, v[132:133]
	v_cvt_pk_bf16_f32 v147, v152, v134
	v_lshl_add_u64 v[152:153], s[2:3], 0, v[132:133]
	v_lshlrev_b32_e32 v156, 1, v193
	v_mov_b32_e32 v157, v169
	v_lshl_add_u64 v[132:133], v[152:153], 0, v[156:157]
	v_mov_b32_e32 v149, v169
	v_lshl_add_u64 v[132:133], v[132:133], 0, v[148:149]
	global_store_dwordx4 v[132:133], v[144:147], off nt
	v_or_b32_e32 v132, 16, v150
	v_ashrrev_i32_e32 v133, 31, v132
	v_lshlrev_b64 v[132:133], 11, v[132:133]
	v_lshl_add_u64 v[132:133], s[22:23], 0, v[132:133]
	v_lshl_add_u64 v[158:159], v[168:169], 2, v[132:133]
	s_waitcnt vmcnt(10)
	v_mov_b32_e32 v132, v196
	v_mov_b32_e32 v133, v197
	v_mov_b32_e32 v134, v198
	v_mov_b32_e32 v135, v199
	v_mov_b32_e32 v140, v200
	v_mov_b32_e32 v141, v201
	v_mov_b32_e32 v142, v202
	v_mov_b32_e32 v143, v203
	s_mov_b32 s100, 0x58000
	s_mov_b32 s101, 0
	v_lshl_add_u64 v[204:205], v[206:207], 0, s[100:101]
	global_load_dwordx4 v[196:199], v[204:205], off offset:16
	global_load_dwordx4 v[200:203], v[204:205], off
	s_and_b64 vcc, exec, s[8:9]
	s_mov_b64 s[10:11], -1
	s_cbranch_vccnz .LBB0_1452
	v_mul_f32_e32 v144, 0xbfb8aa3b, v136
	v_mul_f32_e32 v145, 0xbfb8aa3b, v137
	v_exp_f32_e32 v144, v144
	v_exp_f32_e32 v145, v145
	v_mul_f32_e32 v146, 0xbfb8aa3b, v138
	v_mul_f32_e32 v147, 0xbfb8aa3b, v139
	v_exp_f32_e32 v146, v146
	v_pk_mul_f32 v[144:145], v[52:53], v[144:145]
	v_exp_f32_e32 v147, v147
	v_cvt_pk_bf16_f32 v144, v144, v145
	v_mul_f32_e32 v145, 0xbfb8aa3b, v128
	v_exp_f32_e32 v154, v145
	v_mul_f32_e32 v145, 0xbfb8aa3b, v129
	v_exp_f32_e32 v155, v145
	v_mul_f32_e32 v145, 0xbfb8aa3b, v130
	v_exp_f32_e32 v149, v145
	v_pk_mul_f32 v[146:147], v[54:55], v[146:147]
	s_mov_b64 s[10:11], 0
	v_cvt_pk_bf16_f32 v145, v146, v147
	v_pk_mul_f32 v[146:147], v[48:49], v[154:155]
	v_mul_f32_e32 v154, v50, v149
	v_cvt_pk_bf16_f32 v146, v146, v147
	v_mov_b32_e32 v155, v51

;     __device__ __forceinline__ void operator()(const f32x4 (&acc)[2][2][4][2], const Unit& u, int wr, int wc, int fr, int fq) const {
;     ...
;         } else if (u.pn < 16) {
;             const bool isq = u.pn < 14;
;             const int cb = (u.pn - (isq ? 12 : 14)) * 256;
;             bf16_t* d0 = (bf16_t*)(ws + (isq ? WS_QG : WS_KG));
;             f32x4 bc[2][2];
;     ...
;             BC_LOAD(0, 0);
; #pragma unroll
;             for (int g = 0; g < 16; ++g) {
;                 const int ai = g >> 3, m = (g >> 1) & 3, bj = g & 1;
;                 const int r = row0 + ai * HALF + m * 16;
;                 if (g + 1 < 16) BC_LOAD((g + 1) & 1, g + 1);
;                 {
;                     {
;                         const int col = cb + bj * HALF + lc;
;                         const size_t hoff = ((size_t)((r >> 11) * 4 + (col >> 7)) * SEQ + (r & (SEQ - 1))) * 128 + (col & 127);
;                         const f32x4 b0 = bc[g & 1][0], b1 = bc[g & 1][1];
;                         const f32x4 v0 = acc[ai][bj][m][0], v1 = acc[ai][bj][m][1];
;                         const float L2E = 1.4426950408889634f;
;                         if (isq) {
;                             const float s = 0.08838834764831845f;
;                             u32x4 o; o[0] = cvt_pk_bf16(v0[0] * s * __builtin_amdgcn_exp2f(b0[0] * L2E), v0[1] * s * __builtin_amdgcn_exp2f(b0[1] * L2E));
;                             o[1] = cvt_pk_bf16(v0[2] * s * __builtin_amdgcn_exp2f(b0[2] * L2E), v0[3] * s * __builtin_amdgcn_exp2f(b0[3] * L2E));
;                             o[2] = cvt_pk_bf16(v1[0] * s * __builtin_amdgcn_exp2f(b1[0] * L2E), v1[1] * s * __builtin_amdgcn_exp2f(b1[1] * L2E));
;                             o[3] = cvt_pk_bf16(v1[2] * s * __builtin_amdgcn_exp2f(b1[2] * L2E), v1[3] * s * __builtin_amdgcn_exp2f(b1[3] * L2E));
;                             __builtin_nontemporal_store(o, (u32x4*)(d0 + hoff));
;                         } else {
;                             u32x4 o;
;                             o[0] = cvt_pk_bf16(v0[0] * __builtin_amdgcn_exp2f(-b0[0] * L2E), v0[1] * __builtin_amdgcn_exp2f(-b0[1] * L2E));
;                             o[1] = cvt_pk_bf16(v0[2] * __builtin_amdgcn_exp2f(-b0[2] * L2E), v0[3] * __builtin_amdgcn_exp2f(-b0[3] * L2E));
.LBB0_1454:
	v_mul_f32_e32 v128, s10, v131
	v_exp_f32_e32 v130, v128
	v_add_u32_e32 v128, s18, v151
	v_ashrrev_i32_e32 v129, 31, v128
	v_lshlrev_b64 v[128:129], 19, v[128:129]
	v_mul_f32_e32 v130, v155, v130
	v_cvt_pk_bf16_f32 v147, v154, v130
	v_lshl_add_u64 v[154:155], s[2:3], 0, v[128:129]
	v_mov_b32_e32 v157, v169
	v_lshl_add_u64 v[128:129], v[154:155], 0, v[156:157]
	v_mov_b32_e32 v149, v169
	v_lshl_add_u64 v[128:129], v[128:129], 0, v[148:149]
	global_store_dwordx4 v[128:129], v[144:147], off nt
	s_waitcnt vmcnt(10)
	v_mov_b32_e32 v128, v214
	v_mov_b32_e32 v129, v215
	v_mov_b32_e32 v130, v216
	v_mov_b32_e32 v131, v217
	v_mov_b32_e32 v136, v218
	v_mov_b32_e32 v137, v219
	v_mov_b32_e32 v138, v220
	v_mov_b32_e32 v139, v221
	s_mov_b32 s100, 0x58000
	s_mov_b32 s101, 0
	v_lshl_add_u64 v[204:205], v[206:207], 0, s[100:101]
	global_load_dwordx4 v[214:217], v[204:205], off offset:528
	global_load_dwordx4 v[218:221], v[204:205], off offset:512
	s_nop 0
	s_and_b64 vcc, exec, s[8:9]
	s_mov_b64 s[2:3], -1
	s_cbranch_vccnz .LBB0_1456
	v_mul_f32_e32 v144, 0xbfb8aa3b, v140
	v_mul_f32_e32 v145, 0xbfb8aa3b, v141
	v_exp_f32_e32 v144, v144
	v_exp_f32_e32 v145, v145
	v_mul_f32_e32 v146, 0xbfb8aa3b, v142
	v_mul_f32_e32 v147, 0xbfb8aa3b, v143
	v_exp_f32_e32 v146, v146
	v_pk_mul_f32 v[144:145], v[44:45], v[144:145]
	v_exp_f32_e32 v147, v147
	v_cvt_pk_bf16_f32 v144, v144, v145
	v_mul_f32_e32 v145, 0xbfb8aa3b, v132
	v_exp_f32_e32 v156, v145
	v_mul_f32_e32 v145, 0xbfb8aa3b, v133
	v_exp_f32_e32 v157, v145
	v_mul_f32_e32 v145, 0xbfb8aa3b, v134
	v_exp_f32_e32 v149, v145
	v_pk_mul_f32 v[146:147], v[46:47], v[146:147]
	s_mov_b64 s[2:3], 0
	v_cvt_pk_bf16_f32 v145, v146, v147
	v_pk_mul_f32 v[146:147], v[40:41], v[156:157]
	v_mul_f32_e32 v158, v42, v149
	v_cvt_pk_bf16_f32 v146, v146, v147
	v_mov_b32_e32 v159, v43

;     __device__ __forceinline__ void operator()(const f32x4 (&acc)[2][2][4][2], const Unit& u, int wr, int wc, int fr, int fq) const {
;     ...
;         } else if (u.pn < 16) {
;             const bool isq = u.pn < 14;
;             const int cb = (u.pn - (isq ? 12 : 14)) * 256;
;             bf16_t* d0 = (bf16_t*)(ws + (isq ? WS_QG : WS_KG));
;             f32x4 bc[2][2];
;     ...
;             BC_LOAD(0, 0);
; #pragma unroll
;             for (int g = 0; g < 16; ++g) {
;                 const int ai = g >> 3, m = (g >> 1) & 3, bj = g & 1;
;                 const int r = row0 + ai * HALF + m * 16;
;                 if (g + 1 < 16) BC_LOAD((g + 1) & 1, g + 1);
;                 {
;                     {
;                         const int col = cb + bj * HALF + lc;
;                         const size_t hoff = ((size_t)((r >> 11) * 4 + (col >> 7)) * SEQ + (r & (SEQ - 1))) * 128 + (col & 127);
;                         const f32x4 b0 = bc[g & 1][0], b1 = bc[g & 1][1];
;                         const f32x4 v0 = acc[ai][bj][m][0], v1 = acc[ai][bj][m][1];
;                         const float L2E = 1.4426950408889634f;
;                         if (isq) {
;                             const float s = 0.08838834764831845f;
;                             u32x4 o; o[0] = cvt_pk_bf16(v0[0] * s * __builtin_amdgcn_exp2f(b0[0] * L2E), v0[1] * s * __builtin_amdgcn_exp2f(b0[1] * L2E));
;                             o[1] = cvt_pk_bf16(v0[2] * s * __builtin_amdgcn_exp2f(b0[2] * L2E), v0[3] * s * __builtin_amdgcn_exp2f(b0[3] * L2E));
;                             o[2] = cvt_pk_bf16(v1[0] * s * __builtin_amdgcn_exp2f(b1[0] * L2E), v1[1] * s * __builtin_amdgcn_exp2f(b1[1] * L2E));
;                             o[3] = cvt_pk_bf16(v1[2] * s * __builtin_amdgcn_exp2f(b1[2] * L2E), v1[3] * s * __builtin_amdgcn_exp2f(b1[3] * L2E));
;                             __builtin_nontemporal_store(o, (u32x4*)(d0 + hoff));
;                         } else {
;                             u32x4 o;
;                             o[0] = cvt_pk_bf16(v0[0] * __builtin_amdgcn_exp2f(-b0[0] * L2E), v0[1] * __builtin_amdgcn_exp2f(-b0[1] * L2E));
;                             o[1] = cvt_pk_bf16(v0[2] * __builtin_amdgcn_exp2f(-b0[2] * L2E), v0[3] * __builtin_amdgcn_exp2f(-b0[3] * L2E));
.LBB0_1458:
	v_mul_f32_e32 v132, s2, v135
	v_exp_f32_e32 v132, v132
	v_or_b32_e32 v133, 0x800, v193
	v_mov_b32_e32 v157, v169
	v_lshlrev_b32_e32 v156, 1, v133
	v_mul_f32_e32 v132, v159, v132
	v_cvt_pk_bf16_f32 v147, v158, v132
	v_lshl_add_u64 v[132:133], v[152:153], 0, v[156:157]
	v_mov_b32_e32 v149, v169
	v_lshl_add_u64 v[132:133], v[132:133], 0, v[148:149]
	global_store_dwordx4 v[132:133], v[144:147], off nt
	v_or_b32_e32 v132, 32, v150
	v_ashrrev_i32_e32 v133, 31, v132
	v_lshlrev_b64 v[132:133], 11, v[132:133]
	v_lshl_add_u64 v[132:133], s[22:23], 0, v[132:133]
	v_lshl_add_u64 v[158:159], v[168:169], 2, v[132:133]
	s_waitcnt vmcnt(10)
	v_mov_b32_e32 v132, v222
	v_mov_b32_e32 v133, v223
	v_mov_b32_e32 v134, v224
	v_mov_b32_e32 v135, v225
	v_mov_b32_e32 v140, v226
	v_mov_b32_e32 v141, v227
	v_mov_b32_e32 v142, v228
	v_mov_b32_e32 v143, v229
	s_and_b64 vcc, exec, s[8:9]
	s_mov_b64 s[2:3], -1
	s_cbranch_vccnz .LBB0_1460
	v_mul_f32_e32 v144, 0xbfb8aa3b, v136
	v_mul_f32_e32 v145, 0xbfb8aa3b, v137
	v_exp_f32_e32 v144, v144
	v_exp_f32_e32 v145, v145
	v_mul_f32_e32 v146, 0xbfb8aa3b, v138
	v_mul_f32_e32 v147, 0xbfb8aa3b, v139
	v_exp_f32_e32 v146, v146
	v_pk_mul_f32 v[144:145], v[36:37], v[144:145]
	v_exp_f32_e32 v147, v147
	v_cvt_pk_bf16_f32 v144, v144, v145
	v_mul_f32_e32 v145, 0xbfb8aa3b, v128
	v_exp_f32_e32 v194, v145
	v_mul_f32_e32 v145, 0xbfb8aa3b, v129
	v_exp_f32_e32 v195, v145
	v_mul_f32_e32 v145, 0xbfb8aa3b, v130
	v_exp_f32_e32 v149, v145
	v_pk_mul_f32 v[146:147], v[38:39], v[146:147]
	s_mov_b64 s[2:3], 0
	v_cvt_pk_bf16_f32 v145, v146, v147
	v_pk_mul_f32 v[146:147], v[32:33], v[194:195]
	v_mul_f32_e32 v194, v34, v149
	v_cvt_pk_bf16_f32 v146, v146, v147
	v_mov_b32_e32 v195, v35

;     __device__ __forceinline__ void operator()(const f32x4 (&acc)[2][2][4][2], const Unit& u, int wr, int wc, int fr, int fq) const {
;     ...
;         } else if (u.pn < 16) {
;             const bool isq = u.pn < 14;
;             const int cb = (u.pn - (isq ? 12 : 14)) * 256;
;             bf16_t* d0 = (bf16_t*)(ws + (isq ? WS_QG : WS_KG));
;             f32x4 bc[2][2];
;     ...
;             BC_LOAD(0, 0);
; #pragma unroll
;             for (int g = 0; g < 16; ++g) {
;                 const int ai = g >> 3, m = (g >> 1) & 3, bj = g & 1;
;                 const int r = row0 + ai * HALF + m * 16;
;                 if (g + 1 < 16) BC_LOAD((g + 1) & 1, g + 1);
;                 {
;                     {
;                         const int col = cb + bj * HALF + lc;
;                         const size_t hoff = ((size_t)((r >> 11) * 4 + (col >> 7)) * SEQ + (r & (SEQ - 1))) * 128 + (col & 127);
;                         const f32x4 b0 = bc[g & 1][0], b1 = bc[g & 1][1];
;                         const f32x4 v0 = acc[ai][bj][m][0], v1 = acc[ai][bj][m][1];
;                         const float L2E = 1.4426950408889634f;
;                         if (isq) {
;                             const float s = 0.08838834764831845f;
;                             u32x4 o; o[0] = cvt_pk_bf16(v0[0] * s * __builtin_amdgcn_exp2f(b0[0] * L2E), v0[1] * s * __builtin_amdgcn_exp2f(b0[1] * L2E));
;                             o[1] = cvt_pk_bf16(v0[2] * s * __builtin_amdgcn_exp2f(b0[2] * L2E), v0[3] * s * __builtin_amdgcn_exp2f(b0[3] * L2E));
;                             o[2] = cvt_pk_bf16(v1[0] * s * __builtin_amdgcn_exp2f(b1[0] * L2E), v1[1] * s * __builtin_amdgcn_exp2f(b1[1] * L2E));
;                             o[3] = cvt_pk_bf16(v1[2] * s * __builtin_amdgcn_exp2f(b1[2] * L2E), v1[3] * s * __builtin_amdgcn_exp2f(b1[3] * L2E));
;                             __builtin_nontemporal_store(o, (u32x4*)(d0 + hoff));
;                         } else {
;                             u32x4 o;
;                             o[0] = cvt_pk_bf16(v0[0] * __builtin_amdgcn_exp2f(-b0[0] * L2E), v0[1] * __builtin_amdgcn_exp2f(-b0[1] * L2E));
;                             o[1] = cvt_pk_bf16(v0[2] * __builtin_amdgcn_exp2f(-b0[2] * L2E), v0[3] * __builtin_amdgcn_exp2f(-b0[3] * L2E));
.LBB0_1462:
	v_mul_f32_e32 v128, s2, v131
	v_exp_f32_e32 v130, v128
	v_mov_b32_e32 v157, v169
	v_mov_b32_e32 v149, v169
	v_lshl_add_u64 v[128:129], v[154:155], 0, v[156:157]
	v_mul_f32_e32 v130, v195, v130
	v_cvt_pk_bf16_f32 v147, v194, v130
	v_lshl_add_u64 v[128:129], v[128:129], 0, v[148:149]
	global_store_dwordx4 v[128:129], v[144:147], off nt
	s_waitcnt vmcnt(8)
	v_mov_b32_e32 v128, v230
	v_mov_b32_e32 v129, v231
	v_mov_b32_e32 v130, v232
	v_mov_b32_e32 v131, v233
	v_mov_b32_e32 v136, v234
	v_mov_b32_e32 v137, v235
	v_mov_b32_e32 v138, v236
	v_mov_b32_e32 v139, v237
	s_nop 0
	s_and_b64 vcc, exec, s[8:9]
	s_mov_b64 s[2:3], -1
	s_cbranch_vccnz .LBB0_1464
	v_mul_f32_e32 v144, 0xbfb8aa3b, v140
	v_mul_f32_e32 v145, 0xbfb8aa3b, v141
	v_exp_f32_e32 v144, v144
	v_exp_f32_e32 v145, v145
	v_mul_f32_e32 v146, 0xbfb8aa3b, v142
	v_mul_f32_e32 v147, 0xbfb8aa3b, v143
	v_exp_f32_e32 v146, v146
	v_pk_mul_f32 v[144:145], v[28:29], v[144:145]
	v_exp_f32_e32 v147, v147
	v_cvt_pk_bf16_f32 v144, v144, v145
	v_mul_f32_e32 v145, 0xbfb8aa3b, v132
	v_exp_f32_e32 v156, v145
	v_mul_f32_e32 v145, 0xbfb8aa3b, v133
	v_exp_f32_e32 v157, v145
	v_mul_f32_e32 v145, 0xbfb8aa3b, v134
	v_exp_f32_e32 v149, v145
	v_pk_mul_f32 v[146:147], v[30:31], v[146:147]
	s_mov_b64 s[2:3], 0
	v_cvt_pk_bf16_f32 v145, v146, v147
	v_pk_mul_f32 v[146:147], v[24:25], v[156:157]
	v_mul_f32_e32 v158, v26, v149
	v_cvt_pk_bf16_f32 v146, v146, v147
	v_mov_b32_e32 v159, v27

;     __device__ __forceinline__ void operator()(const f32x4 (&acc)[2][2][4][2], const Unit& u, int wr, int wc, int fr, int fq) const {
;     ...
;         } else if (u.pn < 16) {
;             const bool isq = u.pn < 14;
;             const int cb = (u.pn - (isq ? 12 : 14)) * 256;
;             bf16_t* d0 = (bf16_t*)(ws + (isq ? WS_QG : WS_KG));
;             f32x4 bc[2][2];
;     ...
;             BC_LOAD(0, 0);
; #pragma unroll
;             for (int g = 0; g < 16; ++g) {
;                 const int ai = g >> 3, m = (g >> 1) & 3, bj = g & 1;
;                 const int r = row0 + ai * HALF + m * 16;
;                 if (g + 1 < 16) BC_LOAD((g + 1) & 1, g + 1);
;                 {
;                     {
;                         const int col = cb + bj * HALF + lc;
;                         const size_t hoff = ((size_t)((r >> 11) * 4 + (col >> 7)) * SEQ + (r & (SEQ - 1))) * 128 + (col & 127);
;                         const f32x4 b0 = bc[g & 1][0], b1 = bc[g & 1][1];
;                         const f32x4 v0 = acc[ai][bj][m][0], v1 = acc[ai][bj][m][1];
;                         const float L2E = 1.4426950408889634f;
;                         if (isq) {
;                             const float s = 0.08838834764831845f;
;                             u32x4 o; o[0] = cvt_pk_bf16(v0[0] * s * __builtin_amdgcn_exp2f(b0[0] * L2E), v0[1] * s * __builtin_amdgcn_exp2f(b0[1] * L2E));
;                             o[1] = cvt_pk_bf16(v0[2] * s * __builtin_amdgcn_exp2f(b0[2] * L2E), v0[3] * s * __builtin_amdgcn_exp2f(b0[3] * L2E));
;                             o[2] = cvt_pk_bf16(v1[0] * s * __builtin_amdgcn_exp2f(b1[0] * L2E), v1[1] * s * __builtin_amdgcn_exp2f(b1[1] * L2E));
;                             o[3] = cvt_pk_bf16(v1[2] * s * __builtin_amdgcn_exp2f(b1[2] * L2E), v1[3] * s * __builtin_amdgcn_exp2f(b1[3] * L2E));
;                             __builtin_nontemporal_store(o, (u32x4*)(d0 + hoff));
;                         } else {
;                             u32x4 o;
;                             o[0] = cvt_pk_bf16(v0[0] * __builtin_amdgcn_exp2f(-b0[0] * L2E), v0[1] * __builtin_amdgcn_exp2f(-b0[1] * L2E));
;                             o[1] = cvt_pk_bf16(v0[2] * __builtin_amdgcn_exp2f(-b0[2] * L2E), v0[3] * __builtin_amdgcn_exp2f(-b0[3] * L2E));
.LBB0_1466:
	v_mul_f32_e32 v132, s2, v135
	v_exp_f32_e32 v132, v132
	v_or_b32_e32 v133, 0x1000, v193
	v_mov_b32_e32 v157, v169
	v_lshlrev_b32_e32 v156, 1, v133
	v_mul_f32_e32 v132, v159, v132
	v_cvt_pk_bf16_f32 v147, v158, v132
	v_lshl_add_u64 v[132:133], v[152:153], 0, v[156:157]
	v_mov_b32_e32 v149, v169
	v_lshl_add_u64 v[132:133], v[132:133], 0, v[148:149]
	global_store_dwordx4 v[132:133], v[144:147], off nt
	v_or_b32_e32 v132, 48, v150
	v_ashrrev_i32_e32 v133, 31, v132
	v_lshlrev_b64 v[132:133], 11, v[132:133]
	v_lshl_add_u64 v[132:133], s[22:23], 0, v[132:133]
	v_lshl_add_u64 v[150:151], v[168:169], 2, v[132:133]
	s_waitcnt vmcnt(6)
	v_mov_b32_e32 v132, v196
	v_mov_b32_e32 v133, v197
	v_mov_b32_e32 v134, v198
	v_mov_b32_e32 v135, v199
	v_mov_b32_e32 v140, v200
	v_mov_b32_e32 v141, v201
	v_mov_b32_e32 v142, v202
	v_mov_b32_e32 v143, v203
	s_and_b64 vcc, exec, s[8:9]
	s_mov_b64 s[2:3], -1
	s_cbranch_vccnz .LBB0_1468
	v_mul_f32_e32 v144, 0xbfb8aa3b, v136
	v_mul_f32_e32 v145, 0xbfb8aa3b, v137
	v_exp_f32_e32 v144, v144
	v_exp_f32_e32 v145, v145
	v_mul_f32_e32 v146, 0xbfb8aa3b, v138
	v_mul_f32_e32 v147, 0xbfb8aa3b, v139
	v_exp_f32_e32 v146, v146
	v_pk_mul_f32 v[144:145], v[20:21], v[144:145]
	v_exp_f32_e32 v147, v147
	v_cvt_pk_bf16_f32 v144, v144, v145
	v_mul_f32_e32 v145, 0xbfb8aa3b, v128
	v_exp_f32_e32 v158, v145
	v_mul_f32_e32 v145, 0xbfb8aa3b, v129
	v_exp_f32_e32 v159, v145
	v_mul_f32_e32 v145, 0xbfb8aa3b, v130
	v_exp_f32_e32 v149, v145
	v_pk_mul_f32 v[146:147], v[22:23], v[146:147]
	s_mov_b64 s[2:3], 0
	v_cvt_pk_bf16_f32 v145, v146, v147
	v_pk_mul_f32 v[146:147], v[16:17], v[158:159]
	v_mul_f32_e32 v158, v18, v149
	v_cvt_pk_bf16_f32 v146, v146, v147
	v_mov_b32_e32 v159, v19

;     __device__ __forceinline__ void operator()(const f32x4 (&acc)[2][2][4][2], const Unit& u, int wr, int wc, int fr, int fq) const {
;     ...
;         } else if (u.pn < 16) {
;             const bool isq = u.pn < 14;
;             const int cb = (u.pn - (isq ? 12 : 14)) * 256;
;             bf16_t* d0 = (bf16_t*)(ws + (isq ? WS_QG : WS_KG));
;             f32x4 bc[2][2];
;     ...
;             BC_LOAD(0, 0);
; #pragma unroll
;             for (int g = 0; g < 16; ++g) {
;                 const int ai = g >> 3, m = (g >> 1) & 3, bj = g & 1;
;                 const int r = row0 + ai * HALF + m * 16;
;                 if (g + 1 < 16) BC_LOAD((g + 1) & 1, g + 1);
;                 {
;                     {
;                         const int col = cb + bj * HALF + lc;
;                         const size_t hoff = ((size_t)((r >> 11) * 4 + (col >> 7)) * SEQ + (r & (SEQ - 1))) * 128 + (col & 127);
;                         const f32x4 b0 = bc[g & 1][0], b1 = bc[g & 1][1];
;                         const f32x4 v0 = acc[ai][bj][m][0], v1 = acc[ai][bj][m][1];
;                         const float L2E = 1.4426950408889634f;
;                         if (isq) {
;                             const float s = 0.08838834764831845f;
;                             u32x4 o; o[0] = cvt_pk_bf16(v0[0] * s * __builtin_amdgcn_exp2f(b0[0] * L2E), v0[1] * s * __builtin_amdgcn_exp2f(b0[1] * L2E));
;                             o[1] = cvt_pk_bf16(v0[2] * s * __builtin_amdgcn_exp2f(b0[2] * L2E), v0[3] * s * __builtin_amdgcn_exp2f(b0[3] * L2E));
;                             o[2] = cvt_pk_bf16(v1[0] * s * __builtin_amdgcn_exp2f(b1[0] * L2E), v1[1] * s * __builtin_amdgcn_exp2f(b1[1] * L2E));
;                             o[3] = cvt_pk_bf16(v1[2] * s * __builtin_amdgcn_exp2f(b1[2] * L2E), v1[3] * s * __builtin_amdgcn_exp2f(b1[3] * L2E));
;                             __builtin_nontemporal_store(o, (u32x4*)(d0 + hoff));
;                         } else {
;                             u32x4 o;
;                             o[0] = cvt_pk_bf16(v0[0] * __builtin_amdgcn_exp2f(-b0[0] * L2E), v0[1] * __builtin_amdgcn_exp2f(-b0[1] * L2E));
;                             o[1] = cvt_pk_bf16(v0[2] * __builtin_amdgcn_exp2f(-b0[2] * L2E), v0[3] * __builtin_amdgcn_exp2f(-b0[3] * L2E));
.LBB0_1470:
	v_mul_f32_e32 v128, s2, v131
	v_exp_f32_e32 v130, v128
	v_mov_b32_e32 v157, v169
	v_mov_b32_e32 v149, v169
	v_lshl_add_u64 v[128:129], v[154:155], 0, v[156:157]
	v_mul_f32_e32 v130, v159, v130
	v_cvt_pk_bf16_f32 v147, v158, v130
	v_lshl_add_u64 v[128:129], v[128:129], 0, v[148:149]
	global_store_dwordx4 v[128:129], v[144:147], off nt
	s_waitcnt vmcnt(4)
	v_mov_b32_e32 v128, v214
	v_mov_b32_e32 v129, v215
	v_mov_b32_e32 v130, v216
	v_mov_b32_e32 v131, v217
	v_mov_b32_e32 v136, v218
	v_mov_b32_e32 v137, v219
	v_mov_b32_e32 v138, v220
	v_mov_b32_e32 v139, v221
	s_nop 0
	s_and_b64 vcc, exec, s[8:9]
	s_mov_b64 s[2:3], -1
	s_cbranch_vccnz .LBB0_1472
	v_mul_f32_e32 v144, 0xbfb8aa3b, v140
	v_mul_f32_e32 v145, 0xbfb8aa3b, v141
	v_exp_f32_e32 v144, v144
	v_exp_f32_e32 v145, v145
	v_mul_f32_e32 v146, 0xbfb8aa3b, v142
	v_mul_f32_e32 v147, 0xbfb8aa3b, v143
	v_exp_f32_e32 v146, v146
	v_pk_mul_f32 v[144:145], v[12:13], v[144:145]
	v_exp_f32_e32 v147, v147
	v_cvt_pk_bf16_f32 v144, v144, v145
	v_mul_f32_e32 v145, 0xbfb8aa3b, v132
	v_exp_f32_e32 v150, v145
	v_mul_f32_e32 v145, 0xbfb8aa3b, v133
	v_exp_f32_e32 v151, v145
	v_mul_f32_e32 v145, 0xbfb8aa3b, v134
	v_exp_f32_e32 v149, v145
	v_pk_mul_f32 v[146:147], v[14:15], v[146:147]
	s_mov_b64 s[2:3], 0
	v_cvt_pk_bf16_f32 v145, v146, v147
	v_pk_mul_f32 v[146:147], v[8:9], v[150:151]
	v_mul_f32_e32 v150, v10, v149
	v_cvt_pk_bf16_f32 v146, v146, v147
	v_mov_b32_e32 v151, v11

; __global__ void __launch_bounds__(512, 2) mk_fwd(MkArgs a) {
	.amdhsa_kernel _Z6mk_fwd6MkArgs
		.amdhsa_group_segment_fixed_size 0
		.amdhsa_private_segment_fixed_size 0
		.amdhsa_kernarg_size 432
		.amdhsa_user_sgpr_count 2
		.amdhsa_user_sgpr_dispatch_ptr 0
		.amdhsa_user_sgpr_queue_ptr 0
		.amdhsa_user_sgpr_kernarg_segment_ptr 1
		.amdhsa_user_sgpr_dispatch_id 0
		.amdhsa_user_sgpr_kernarg_preload_length 0
		.amdhsa_user_sgpr_kernarg_preload_offset 0
		.amdhsa_user_sgpr_private_segment_size 0
		.amdhsa_uses_dynamic_stack 0
		.amdhsa_enable_private_segment 0
		.amdhsa_system_sgpr_workgroup_id_x 1
		.amdhsa_system_sgpr_workgroup_id_y 0
		.amdhsa_system_sgpr_workgroup_id_z 0
		.amdhsa_system_sgpr_workgroup_info 0
		.amdhsa_system_vgpr_workitem_id 0
		.amdhsa_next_free_vgpr 253
		.amdhsa_next_free_sgpr 102
		.amdhsa_accum_offset 256
		.amdhsa_reserve_vcc 1
		.amdhsa_float_round_mode_32 0
		.amdhsa_float_round_mode_16_64 0
		.amdhsa_float_denorm_mode_32 3
		.amdhsa_float_denorm_mode_16_64 3
		.amdhsa_dx10_clamp 1
		.amdhsa_ieee_mode 1
		.amdhsa_fp16_overflow 0
		.amdhsa_tg_split 0
		.amdhsa_exception_fp_ieee_invalid_op 0
		.amdhsa_exception_fp_denorm_src 0
		.amdhsa_exception_fp_ieee_div_zero 0
		.amdhsa_exception_fp_ieee_overflow 0
		.amdhsa_exception_fp_ieee_underflow 0
		.amdhsa_exception_fp_ieee_inexact 0
		.amdhsa_exception_int_div_zero 0
	.end_amdhsa_kernel

; __global__ void __launch_bounds__(512, 2) mk_fwd(MkArgs a) {
amdhsa.kernels:
  - .agpr_count:     0
    .args:
      - .offset:         0
        .size:           176
        .value_kind:     by_value
      - .offset:         176
        .size:           4
        .value_kind:     hidden_block_count_x
      - .offset:         180
        .size:           4
        .value_kind:     hidden_block_count_y
      - .offset:         184
        .size:           4
        .value_kind:     hidden_block_count_z
      - .offset:         188
        .size:           2
        .value_kind:     hidden_group_size_x
      - .offset:         190
        .size:           2
        .value_kind:     hidden_group_size_y
      - .offset:         192
        .size:           2
        .value_kind:     hidden_group_size_z
      - .offset:         194
        .size:           2
        .value_kind:     hidden_remainder_x
      - .offset:         196
        .size:           2
        .value_kind:     hidden_remainder_y
      - .offset:         198
        .size:           2
        .value_kind:     hidden_remainder_z
      - .offset:         216
        .size:           8
        .value_kind:     hidden_global_offset_x
      - .offset:         224
        .size:           8
        .value_kind:     hidden_global_offset_y
      - .offset:         232
        .size:           8
        .value_kind:     hidden_global_offset_z
      - .offset:         240
        .size:           2
        .value_kind:     hidden_grid_dims
      - .offset:         296
        .size:           4
        .value_kind:     hidden_dynamic_lds_size
    .group_segment_fixed_size: 0
    .kernarg_segment_align: 8
    .kernarg_segment_size: 432
    .language:       OpenCL C
    .language_version:
      - 2
      - 0
    .max_flat_workgroup_size: 512
    .name:           _Z6mk_fwd6MkArgs
    .private_segment_fixed_size: 0
    .sgpr_count:     108
    .sgpr_spill_count: 61
    .symbol:         _Z6mk_fwd6MkArgs.kd
    .uniform_work_group_size: 1
    .uses_dynamic_stack: false
    .vgpr_count:     253
    .vgpr_spill_count: 0
    .wavefront_size: 64
